# v14 + P13 EpiFin row-sum cross-row shuffles via v_permlane16_swap/v_permlane32_swap instead of ds_bpermute round trips (same add order)
# speedup vs baseline: 1.0096x; 1.0096x over previous
.LBB0_1482:
	s_lshl_b32 s2, s5, 5
	s_lshl_b32 s1, s0, 8
	s_lshl_b32 s3, s4, 8
	s_or_b32 s2, s3, s2
	v_add_u32_e32 v18, s1, v189
	v_or_b32_e32 v2, s2, v1
	v_ashrrev_i32_e32 v19, 31, v18
	v_ashrrev_i32_e32 v3, 31, v2
	v_lshlrev_b64 v[4:5], 11, v[18:19]
	v_lshl_add_u64 v[20:21], v[4:5], 0, v[2:3]
	v_lshlrev_b64 v[4:5], 1, v[20:21]
	v_lshl_add_u64 v[14:15], s[18:19], 0, v[4:5]
	s_barrier
	global_load_dwordx4 v[6:9], v[14:15], off
	v_lshl_add_u64 v[4:5], s[16:17], 0, v[4:5]
	global_load_dwordx4 v[10:13], v[4:5], off
	s_nop 0
	global_load_dwordx4 v[14:17], v[14:15], off offset:256
	s_nop 0
	global_load_dwordx4 v[30:33], v[4:5], off offset:256
	v_lshlrev_b64 v[254:255], 11, v[18:19]
	v_lshl_add_u64 v[254:255], v[254:255], 0, v[2:3]
	v_lshlrev_b64 v[254:255], 1, v[254:255]
	v_mov_b32_e32 v250, 0x10000
	v_mov_b32_e32 v251, 0
	v_lshl_add_u64 v[196:197], s[16:17], 0, v[254:255]
	v_lshl_add_u64 v[254:255], s[18:19], 0, v[254:255]
	v_lshl_add_u64 v[254:255], v[254:255], 0, v[250:251]
	v_lshl_add_u64 v[196:197], v[196:197], 0, v[250:251]
	global_load_dwordx4 v[200:203], v[254:255], off
	global_load_dwordx4 v[204:207], v[196:197], off
	global_load_dwordx4 v[208:211], v[254:255], off offset:256
	global_load_dwordx4 v[212:215], v[196:197], off offset:256
	v_lshl_add_u64 v[254:255], v[254:255], 0, v[250:251]
	v_lshl_add_u64 v[196:197], v[196:197], 0, v[250:251]
	global_load_dwordx4 v[216:219], v[254:255], off
	global_load_dwordx4 v[220:223], v[196:197], off
	global_load_dwordx4 v[224:227], v[254:255], off offset:256
	global_load_dwordx4 v[228:231], v[196:197], off offset:256
	v_lshl_add_u64 v[254:255], v[254:255], 0, v[250:251]
	v_lshl_add_u64 v[196:197], v[196:197], 0, v[250:251]
	global_load_dwordx4 v[232:235], v[254:255], off
	global_load_dwordx4 v[236:239], v[196:197], off
	global_load_dwordx4 v[240:243], v[254:255], off offset:256
	global_load_dwordx4 v[244:247], v[196:197], off offset:256
	v_mbcnt_lo_u32_b32 v4, -1, 0
	s_mov_b32 s6, 0x3c800000
	s_mov_b32 s2, 0xbfb8aa3b
	v_mbcnt_hi_u32_b32 v163, -1, v4
	v_pk_mul_f32 v[4:5], v[160:161], s[6:7] op_sel_hi:[1,0]
	v_pk_mul_f32 v[22:23], v[158:159], s[6:7] op_sel_hi:[1,0]
	v_pk_mul_f32 v[24:25], v[156:157], s[6:7] op_sel_hi:[1,0]
	v_pk_mul_f32 v[26:27], v[154:155], s[6:7] op_sel_hi:[1,0]
	v_and_b32_e32 v28, 64, v163
	v_pk_mul_f32 v[22:23], v[22:23], s[2:3] op_sel_hi:[1,0]
	v_pk_mul_f32 v[4:5], v[4:5], s[2:3] op_sel_hi:[1,0]
	v_pk_mul_f32 v[26:27], v[26:27], s[2:3] op_sel_hi:[1,0]
	v_pk_mul_f32 v[24:25], v[24:25], s[2:3] op_sel_hi:[1,0]
	v_add_u32_e32 v165, 64, v28
	v_exp_f32_e32 v22, v22
	v_exp_f32_e32 v23, v23
	v_exp_f32_e32 v28, v4
	v_exp_f32_e32 v29, v5
	v_exp_f32_e32 v26, v26
	v_exp_f32_e32 v27, v27
	v_exp_f32_e32 v24, v24
	v_exp_f32_e32 v25, v25
	v_xor_b32_e32 v154, 16, v163
	v_cmp_lt_i32_e32 vcc, v154, v165
	v_pk_add_f32 v[22:23], v[22:23], 1.0 op_sel_hi:[1,0]
	v_pk_add_f32 v[28:29], v[28:29], 1.0 op_sel_hi:[1,0]
	v_pk_add_f32 v[26:27], v[26:27], 1.0 op_sel_hi:[1,0]
	v_pk_add_f32 v[24:25], v[24:25], 1.0 op_sel_hi:[1,0]
	v_cndmask_b32_e32 v4, v163, v154, vcc
	v_rcp_f32_e32 v22, v22
	v_rcp_f32_e32 v23, v23
	v_rcp_f32_e32 v28, v28
	v_rcp_f32_e32 v29, v29
	v_rcp_f32_e32 v26, v26
	v_rcp_f32_e32 v27, v27
	v_rcp_f32_e32 v154, v24
	v_rcp_f32_e32 v155, v25
	v_pk_mul_f32 v[148:149], v[148:149], s[6:7] op_sel_hi:[1,0]
	v_pk_mul_f32 v[146:147], v[146:147], s[6:7] op_sel_hi:[1,0]
	v_pk_mul_f32 v[148:149], v[148:149], s[2:3] op_sel_hi:[1,0]
	v_pk_mul_f32 v[146:147], v[146:147], s[2:3] op_sel_hi:[1,0]
	v_exp_f32_e32 v148, v148
	v_exp_f32_e32 v149, v149
	v_exp_f32_e32 v146, v146
	v_exp_f32_e32 v147, v147
	v_lshlrev_b32_e32 v4, 2, v4
	v_pk_add_f32 v[148:149], v[148:149], 1.0 op_sel_hi:[1,0]
	v_pk_add_f32 v[146:147], v[146:147], 1.0 op_sel_hi:[1,0]
	v_rcp_f32_e32 v148, v148
	v_rcp_f32_e32 v149, v149
	s_waitcnt vmcnt(12)
	v_lshlrev_b32_e32 v160, 16, v10
	v_lshlrev_b32_e32 v156, 16, v6
	v_and_b32_e32 v157, 0xffff0000, v6
	v_lshlrev_b32_e32 v6, 16, v7
	v_and_b32_e32 v7, 0xffff0000, v7
	v_lshlrev_b32_e32 v158, 16, v8
	v_and_b32_e32 v159, 0xffff0000, v8
	v_lshlrev_b32_e32 v8, 16, v9
	v_and_b32_e32 v9, 0xffff0000, v9
	v_and_b32_e32 v161, 0xffff0000, v10
	v_lshlrev_b32_e32 v10, 16, v11
	v_and_b32_e32 v11, 0xffff0000, v11
	v_lshlrev_b32_e32 v170, 16, v12
	v_and_b32_e32 v171, 0xffff0000, v12
	v_lshlrev_b32_e32 v12, 16, v13
	v_and_b32_e32 v13, 0xffff0000, v13
	v_pk_fma_f32 v[24:25], v[28:29], v[6:7], v[10:11]
	v_pk_fma_f32 v[28:29], v[22:23], v[156:157], v[160:161]
	v_pk_fma_f32 v[22:23], v[154:155], v[8:9], v[12:13]
	v_pk_fma_f32 v[26:27], v[26:27], v[158:159], v[170:171]
	v_mul_f32_e32 v5, v29, v29
	v_mul_f32_e32 v6, v25, v25
	v_mul_f32_e32 v7, v27, v27
	v_mul_f32_e32 v8, v23, v23
	v_fmac_f32_e32 v5, v28, v28
	v_fmac_f32_e32 v6, v24, v24
	v_fmac_f32_e32 v7, v26, v26
	v_fmac_f32_e32 v8, v22, v22
	v_add_f32_e32 v5, v5, v6
	v_add_f32_e32 v6, v7, v8
	v_lshlrev_b32_e32 v174, 16, v16
	v_and_b32_e32 v175, 0xffff0000, v16
	v_add_f32_e32 v5, v5, v6
	v_lshlrev_b32_e32 v6, 16, v17
	v_and_b32_e32 v7, 0xffff0000, v17
	v_lshlrev_b32_e32 v8, 16, v30
	v_and_b32_e32 v9, 0xffff0000, v30
	v_lshlrev_b32_e32 v10, 16, v31
	v_and_b32_e32 v11, 0xffff0000, v31
	v_lshlrev_b32_e32 v12, 16, v32
	v_and_b32_e32 v13, 0xffff0000, v32
	v_lshlrev_b32_e32 v16, 16, v33
	v_and_b32_e32 v17, 0xffff0000, v33
	v_pk_mul_f32 v[30:31], v[152:153], s[6:7] op_sel_hi:[1,0]
	v_pk_mul_f32 v[32:33], v[150:151], s[6:7] op_sel_hi:[1,0]
	v_pk_mul_f32 v[30:31], v[30:31], s[2:3] op_sel_hi:[1,0]
	v_pk_mul_f32 v[32:33], v[32:33], s[2:3] op_sel_hi:[1,0]
	v_exp_f32_e32 v30, v30
	v_exp_f32_e32 v32, v32
	v_exp_f32_e32 v33, v33
	v_exp_f32_e32 v31, v31
	v_rcp_f32_e32 v150, v146
	v_rcp_f32_e32 v151, v147
	v_pk_add_f32 v[32:33], v[32:33], 1.0 op_sel_hi:[1,0]
	v_pk_add_f32 v[30:31], v[30:31], 1.0 op_sel_hi:[1,0]
	v_rcp_f32_e32 v32, v32
	v_rcp_f32_e32 v33, v33
	v_rcp_f32_e32 v30, v30
	v_rcp_f32_e32 v31, v31
	v_lshlrev_b32_e32 v172, 16, v14
	v_and_b32_e32 v173, 0xffff0000, v14
	v_lshlrev_b32_e32 v14, 16, v15
	v_and_b32_e32 v15, 0xffff0000, v15
	v_pk_fma_f32 v[30:31], v[30:31], v[14:15], v[10:11]
	v_pk_fma_f32 v[32:33], v[32:33], v[172:173], v[8:9]
	v_pk_fma_f32 v[146:147], v[148:149], v[6:7], v[16:17]
	v_mul_f32_e32 v6, v33, v33
	v_mul_f32_e32 v7, v31, v31
	v_pk_fma_f32 v[148:149], v[150:151], v[174:175], v[12:13]
	v_fmac_f32_e32 v6, v32, v32
	v_fmac_f32_e32 v7, v30, v30
	v_add_f32_e32 v6, v6, v7
	v_mul_f32_e32 v7, v149, v149
	v_mul_f32_e32 v8, v147, v147
	v_fmac_f32_e32 v7, v148, v148
	v_fmac_f32_e32 v8, v146, v146
	v_add_f32_e32 v7, v7, v8
	v_add_f32_e32 v6, v6, v7
	v_add_f32_e32 v5, v5, v6
	v_mov_b32_e32 v7, v5
	s_nop 1
	v_permlane16_swap_b32 v7, v5
	s_nop 0
	v_xor_b32_e32 v6, 32, v163
	v_cmp_lt_i32_e32 vcc, v6, v165
	s_lshl_b32 s3, s5, 2
	s_add_i32 s5, s3, 0
	v_cndmask_b32_e32 v6, v163, v6, vcc
	v_lshlrev_b32_e32 v6, 2, v6
	s_waitcnt lgkmcnt(0)
	v_add_f32_e32 v7, v5, v7
	v_mov_b32_e32 v8, v7
	s_nop 1
	v_permlane32_swap_b32 v8, v7
	s_nop 0
	v_cmp_gt_u32_e32 vcc, 16, v198
	v_lshl_add_u32 v5, v189, 4, s5
	s_and_saveexec_b64 s[20:21], vcc
	s_cbranch_execz .LBB0_1484
	s_waitcnt lgkmcnt(0)
	v_add_f32_e32 v7, v7, v8
	ds_write_b32 v5, v7
.LBB0_1484:
	s_or_b64 exec, exec, s[20:21]
	s_waitcnt lgkmcnt(0)
	s_waitcnt vmcnt(8)
	v_mov_b64_e32 v[8:9], v[200:201]
	v_mov_b64_e32 v[10:11], v[202:203]
	v_mov_b64_e32 v[12:13], v[204:205]
	v_mov_b64_e32 v[14:15], v[206:207]
	v_mov_b64_e32 v[150:151], v[208:209]
	v_mov_b64_e32 v[152:153], v[210:211]
	v_mov_b64_e32 v[154:155], v[212:213]
	v_mov_b64_e32 v[156:157], v[214:215]
	v_lshl_add_u64 v[254:255], v[254:255], 0, v[250:251]
	v_lshl_add_u64 v[196:197], v[196:197], 0, v[250:251]
	v_lshl_add_u64 v[254:255], v[254:255], 0, v[250:251]
	v_lshl_add_u64 v[196:197], v[196:197], 0, v[250:251]
	v_lshl_add_u64 v[254:255], v[254:255], 0, v[250:251]
	v_lshl_add_u64 v[196:197], v[196:197], 0, v[250:251]
	v_lshl_add_u64 v[254:255], v[254:255], 0, v[250:251]
	v_lshl_add_u64 v[196:197], v[196:197], 0, v[250:251]
	v_lshl_add_u64 v[254:255], v[254:255], 0, v[250:251]
	v_lshl_add_u64 v[196:197], v[196:197], 0, v[250:251]
	global_load_dwordx4 v[200:203], v[254:255], off
	global_load_dwordx4 v[204:207], v[196:197], off
	global_load_dwordx4 v[208:211], v[254:255], off offset:256
	global_load_dwordx4 v[212:215], v[196:197], off offset:256
	v_pk_mul_f32 v[16:17], v[144:145], s[6:7] op_sel_hi:[1,0]
	v_pk_mul_f32 v[142:143], v[142:143], s[6:7] op_sel_hi:[1,0]
	v_pk_mul_f32 v[140:141], v[140:141], s[6:7] op_sel_hi:[1,0]
	v_pk_mul_f32 v[138:139], v[138:139], s[6:7] op_sel_hi:[1,0]
	v_pk_mul_f32 v[136:137], v[136:137], s[6:7] op_sel_hi:[1,0]
	v_pk_mul_f32 v[142:143], v[142:143], s[2:3] op_sel_hi:[1,0]
	v_pk_mul_f32 v[16:17], v[16:17], s[2:3] op_sel_hi:[1,0]
	v_pk_mul_f32 v[138:139], v[138:139], s[2:3] op_sel_hi:[1,0]
	v_pk_mul_f32 v[140:141], v[140:141], s[2:3] op_sel_hi:[1,0]
	v_pk_mul_f32 v[144:145], v[136:137], s[2:3] op_sel_hi:[1,0]
	v_exp_f32_e32 v136, v142
	v_exp_f32_e32 v137, v143
	v_exp_f32_e32 v16, v16
	v_exp_f32_e32 v17, v17
	v_exp_f32_e32 v138, v138
	v_exp_f32_e32 v139, v139
	v_exp_f32_e32 v140, v140
	v_exp_f32_e32 v141, v141
	v_pk_mul_f32 v[134:135], v[134:135], s[6:7] op_sel_hi:[1,0]
	v_pk_add_f32 v[16:17], v[16:17], 1.0 op_sel_hi:[1,0]
	v_pk_mul_f32 v[134:135], v[134:135], s[2:3] op_sel_hi:[1,0]
	v_rcp_f32_e32 v16, v16
	v_exp_f32_e32 v142, v134
	v_exp_f32_e32 v143, v135
	v_pk_add_f32 v[134:135], v[136:137], 1.0 op_sel_hi:[1,0]
	v_pk_add_f32 v[136:137], v[138:139], 1.0 op_sel_hi:[1,0]
	v_pk_add_f32 v[138:139], v[140:141], 1.0 op_sel_hi:[1,0]
	v_rcp_f32_e32 v134, v134
	v_rcp_f32_e32 v135, v135
	v_rcp_f32_e32 v17, v17
	v_rcp_f32_e32 v158, v136
	v_rcp_f32_e32 v159, v137
	v_rcp_f32_e32 v138, v138
	v_rcp_f32_e32 v139, v139
	v_lshlrev_b32_e32 v170, 16, v12
	v_lshlrev_b32_e32 v140, 16, v8
	v_and_b32_e32 v141, 0xffff0000, v8
	v_lshlrev_b32_e32 v8, 16, v9
	v_and_b32_e32 v9, 0xffff0000, v9
	v_lshlrev_b32_e32 v160, 16, v10
	v_and_b32_e32 v161, 0xffff0000, v10
	v_lshlrev_b32_e32 v10, 16, v11
	v_and_b32_e32 v11, 0xffff0000, v11
	v_and_b32_e32 v171, 0xffff0000, v12
	v_lshlrev_b32_e32 v12, 16, v13
	v_and_b32_e32 v13, 0xffff0000, v13
	v_lshlrev_b32_e32 v172, 16, v14
	v_and_b32_e32 v173, 0xffff0000, v14
	v_lshlrev_b32_e32 v14, 16, v15
	v_and_b32_e32 v15, 0xffff0000, v15
	v_pk_fma_f32 v[136:137], v[16:17], v[8:9], v[12:13]
	v_pk_fma_f32 v[140:141], v[134:135], v[140:141], v[170:171]
	v_pk_fma_f32 v[134:135], v[138:139], v[10:11], v[14:15]
	v_pk_fma_f32 v[138:139], v[158:159], v[160:161], v[172:173]
	v_mul_f32_e32 v7, v141, v141
	v_mul_f32_e32 v8, v137, v137
	v_mul_f32_e32 v9, v139, v139
	v_mul_f32_e32 v10, v135, v135
	v_fmac_f32_e32 v7, v140, v140
	v_fmac_f32_e32 v8, v136, v136
	v_fmac_f32_e32 v9, v138, v138
	v_fmac_f32_e32 v10, v134, v134
	v_add_f32_e32 v7, v7, v8
	v_add_f32_e32 v8, v9, v10
	v_add_f32_e32 v7, v7, v8
	v_exp_f32_e32 v8, v144
	v_exp_f32_e32 v9, v145
	v_pk_mul_f32 v[12:13], v[132:133], s[6:7] op_sel_hi:[1,0]
	v_pk_mul_f32 v[14:15], v[130:131], s[6:7] op_sel_hi:[1,0]
	v_pk_mul_f32 v[12:13], v[12:13], s[2:3] op_sel_hi:[1,0]
	v_pk_mul_f32 v[14:15], v[14:15], s[2:3] op_sel_hi:[1,0]
	v_exp_f32_e32 v12, v12
	v_exp_f32_e32 v14, v14
	v_exp_f32_e32 v15, v15
	v_exp_f32_e32 v13, v13
	v_pk_add_f32 v[10:11], v[142:143], 1.0 op_sel_hi:[1,0]
	v_pk_add_f32 v[8:9], v[8:9], 1.0 op_sel_hi:[1,0]
	v_rcp_f32_e32 v10, v10
	v_rcp_f32_e32 v11, v11
	v_rcp_f32_e32 v8, v8
	v_rcp_f32_e32 v9, v9
	v_pk_add_f32 v[14:15], v[14:15], 1.0 op_sel_hi:[1,0]
	v_pk_add_f32 v[12:13], v[12:13], 1.0 op_sel_hi:[1,0]
	v_rcp_f32_e32 v14, v14
	v_rcp_f32_e32 v12, v12
	v_rcp_f32_e32 v13, v13
	v_rcp_f32_e32 v15, v15
	v_lshlrev_b32_e32 v174, 16, v150
	v_and_b32_e32 v175, 0xffff0000, v150
	v_lshlrev_b32_e32 v150, 16, v151
	v_and_b32_e32 v151, 0xffff0000, v151
	v_lshlrev_b32_e32 v178, 16, v154
	v_and_b32_e32 v179, 0xffff0000, v154
	v_lshlrev_b32_e32 v154, 16, v155
	v_and_b32_e32 v155, 0xffff0000, v155
	v_pk_fma_f32 v[130:131], v[8:9], v[150:151], v[154:155]
	v_pk_fma_f32 v[132:133], v[10:11], v[174:175], v[178:179]
	v_lshlrev_b32_e32 v176, 16, v152
	v_and_b32_e32 v177, 0xffff0000, v152
	v_lshlrev_b32_e32 v152, 16, v153
	v_and_b32_e32 v153, 0xffff0000, v153
	v_lshlrev_b32_e32 v180, 16, v156
	v_and_b32_e32 v181, 0xffff0000, v156
	v_lshlrev_b32_e32 v156, 16, v157
	v_and_b32_e32 v157, 0xffff0000, v157
	v_mul_f32_e32 v8, v133, v133
	v_mul_f32_e32 v9, v131, v131
	v_pk_fma_f32 v[142:143], v[12:13], v[152:153], v[156:157]
	v_pk_fma_f32 v[144:145], v[14:15], v[176:177], v[180:181]
	v_fmac_f32_e32 v8, v132, v132
	v_fmac_f32_e32 v9, v130, v130
	v_add_f32_e32 v8, v8, v9
	v_mul_f32_e32 v9, v145, v145
	v_mul_f32_e32 v10, v143, v143
	v_fmac_f32_e32 v9, v144, v144
	v_fmac_f32_e32 v10, v142, v142
	v_add_f32_e32 v9, v9, v10
	v_add_f32_e32 v8, v8, v9
	v_add_f32_e32 v7, v7, v8
	v_mov_b32_e32 v8, v7
	s_nop 1
	v_permlane16_swap_b32 v8, v7
	s_nop 0
	s_waitcnt lgkmcnt(0)
	v_add_f32_e32 v7, v7, v8
	v_mov_b32_e32 v8, v7
	s_nop 1
	v_permlane32_swap_b32 v8, v7
	s_nop 0
	s_and_saveexec_b64 s[2:3], vcc
	s_cbranch_execz .LBB0_1486
	s_waitcnt lgkmcnt(0)
	v_add_f32_e32 v7, v7, v8
	ds_write_b32 v5, v7 offset:256
.LBB0_1486:
	s_or_b64 exec, exec, s[2:3]
	s_waitcnt lgkmcnt(0)
	s_waitcnt vmcnt(8)
	v_mov_b64_e32 v[8:9], v[216:217]
	v_mov_b64_e32 v[10:11], v[218:219]
	v_mov_b64_e32 v[12:13], v[220:221]
	v_mov_b64_e32 v[14:15], v[222:223]
	v_mov_b64_e32 v[150:151], v[224:225]
	v_mov_b64_e32 v[152:153], v[226:227]
	v_mov_b64_e32 v[154:155], v[228:229]
	v_mov_b64_e32 v[156:157], v[230:231]
	v_lshl_add_u64 v[254:255], v[254:255], 0, v[250:251]
	v_lshl_add_u64 v[196:197], v[196:197], 0, v[250:251]
	global_load_dwordx4 v[216:219], v[254:255], off
	global_load_dwordx4 v[220:223], v[196:197], off
	global_load_dwordx4 v[224:227], v[254:255], off offset:256
	global_load_dwordx4 v[228:231], v[196:197], off offset:256
	s_mov_b32 s2, 0xbfb8aa3b
	v_pk_mul_f32 v[16:17], v[128:129], s[6:7] op_sel_hi:[1,0]
	v_pk_mul_f32 v[126:127], v[126:127], s[6:7] op_sel_hi:[1,0]
	v_pk_mul_f32 v[124:125], v[124:125], s[6:7] op_sel_hi:[1,0]
	v_pk_mul_f32 v[122:123], v[122:123], s[6:7] op_sel_hi:[1,0]
	v_pk_mul_f32 v[128:129], v[120:121], s[6:7] op_sel_hi:[1,0]
	v_pk_mul_f32 v[118:119], v[118:119], s[6:7] op_sel_hi:[1,0]
	v_pk_mul_f32 v[120:121], v[126:127], s[2:3] op_sel_hi:[1,0]
	v_pk_mul_f32 v[16:17], v[16:17], s[2:3] op_sel_hi:[1,0]
	v_pk_mul_f32 v[122:123], v[122:123], s[2:3] op_sel_hi:[1,0]
	v_pk_mul_f32 v[124:125], v[124:125], s[2:3] op_sel_hi:[1,0]
	v_pk_mul_f32 v[126:127], v[118:119], s[2:3] op_sel_hi:[1,0]
	v_exp_f32_e32 v118, v120
	v_exp_f32_e32 v119, v121
	v_exp_f32_e32 v16, v16
	v_exp_f32_e32 v17, v17
	v_exp_f32_e32 v120, v122
	v_exp_f32_e32 v121, v123
	v_exp_f32_e32 v122, v124
	v_exp_f32_e32 v123, v125
	v_pk_add_f32 v[118:119], v[118:119], 1.0 op_sel_hi:[1,0]
	v_pk_add_f32 v[16:17], v[16:17], 1.0 op_sel_hi:[1,0]
	v_pk_add_f32 v[120:121], v[120:121], 1.0 op_sel_hi:[1,0]
	v_pk_add_f32 v[122:123], v[122:123], 1.0 op_sel_hi:[1,0]
	v_rcp_f32_e32 v118, v118
	v_rcp_f32_e32 v119, v119
	v_rcp_f32_e32 v16, v16
	v_rcp_f32_e32 v17, v17
	v_rcp_f32_e32 v158, v120
	v_rcp_f32_e32 v159, v121
	v_rcp_f32_e32 v122, v122
	v_rcp_f32_e32 v123, v123
	v_exp_f32_e32 v126, v126
	v_exp_f32_e32 v127, v127
	v_lshlrev_b32_e32 v170, 16, v12
	v_lshlrev_b32_e32 v124, 16, v8
	v_and_b32_e32 v125, 0xffff0000, v8
	v_lshlrev_b32_e32 v8, 16, v9
	v_and_b32_e32 v9, 0xffff0000, v9
	v_lshlrev_b32_e32 v160, 16, v10
	v_and_b32_e32 v161, 0xffff0000, v10
	v_lshlrev_b32_e32 v10, 16, v11
	v_and_b32_e32 v11, 0xffff0000, v11
	v_and_b32_e32 v171, 0xffff0000, v12
	v_lshlrev_b32_e32 v12, 16, v13
	v_and_b32_e32 v13, 0xffff0000, v13
	v_lshlrev_b32_e32 v172, 16, v14
	v_and_b32_e32 v173, 0xffff0000, v14
	v_lshlrev_b32_e32 v14, 16, v15
	v_and_b32_e32 v15, 0xffff0000, v15
	v_pk_fma_f32 v[120:121], v[16:17], v[8:9], v[12:13]
	v_pk_fma_f32 v[124:125], v[118:119], v[124:125], v[170:171]
	v_pk_fma_f32 v[118:119], v[122:123], v[10:11], v[14:15]
	v_pk_fma_f32 v[122:123], v[158:159], v[160:161], v[172:173]
	v_mul_f32_e32 v7, v125, v125
	v_mul_f32_e32 v8, v121, v121
	v_mul_f32_e32 v9, v123, v123
	v_mul_f32_e32 v10, v119, v119
	v_fmac_f32_e32 v7, v124, v124
	v_fmac_f32_e32 v8, v120, v120
	v_fmac_f32_e32 v9, v122, v122
	v_fmac_f32_e32 v10, v118, v118
	v_add_f32_e32 v7, v7, v8
	v_add_f32_e32 v8, v9, v10
	v_add_f32_e32 v7, v7, v8
	v_pk_mul_f32 v[8:9], v[128:129], s[2:3] op_sel_hi:[1,0]
	v_pk_mul_f32 v[12:13], v[116:117], s[6:7] op_sel_hi:[1,0]
	v_exp_f32_e32 v8, v8
	v_exp_f32_e32 v9, v9
	v_pk_mul_f32 v[14:15], v[114:115], s[6:7] op_sel_hi:[1,0]
	v_pk_mul_f32 v[12:13], v[12:13], s[2:3] op_sel_hi:[1,0]
	v_pk_mul_f32 v[14:15], v[14:15], s[2:3] op_sel_hi:[1,0]
	v_exp_f32_e32 v12, v12
	v_exp_f32_e32 v14, v14
	v_exp_f32_e32 v15, v15
	v_exp_f32_e32 v13, v13
	v_pk_add_f32 v[10:11], v[126:127], 1.0 op_sel_hi:[1,0]
	v_pk_add_f32 v[8:9], v[8:9], 1.0 op_sel_hi:[1,0]
	v_rcp_f32_e32 v10, v10
	v_rcp_f32_e32 v11, v11
	v_rcp_f32_e32 v8, v8
	v_rcp_f32_e32 v9, v9
	v_pk_add_f32 v[14:15], v[14:15], 1.0 op_sel_hi:[1,0]
	v_pk_add_f32 v[12:13], v[12:13], 1.0 op_sel_hi:[1,0]
	v_rcp_f32_e32 v14, v14
	v_rcp_f32_e32 v12, v12
	v_rcp_f32_e32 v13, v13
	v_rcp_f32_e32 v15, v15
	v_lshlrev_b32_e32 v174, 16, v150
	v_and_b32_e32 v175, 0xffff0000, v150
	v_lshlrev_b32_e32 v150, 16, v151
	v_and_b32_e32 v151, 0xffff0000, v151
	v_lshlrev_b32_e32 v178, 16, v154
	v_and_b32_e32 v179, 0xffff0000, v154
	v_lshlrev_b32_e32 v154, 16, v155
	v_and_b32_e32 v155, 0xffff0000, v155
	v_pk_fma_f32 v[114:115], v[8:9], v[150:151], v[154:155]
	v_pk_fma_f32 v[116:117], v[10:11], v[174:175], v[178:179]
	v_lshlrev_b32_e32 v176, 16, v152
	v_and_b32_e32 v177, 0xffff0000, v152
	v_lshlrev_b32_e32 v152, 16, v153
	v_and_b32_e32 v153, 0xffff0000, v153
	v_lshlrev_b32_e32 v180, 16, v156
	v_and_b32_e32 v181, 0xffff0000, v156
	v_lshlrev_b32_e32 v156, 16, v157
	v_and_b32_e32 v157, 0xffff0000, v157
	v_mul_f32_e32 v8, v117, v117
	v_mul_f32_e32 v9, v115, v115
	v_pk_fma_f32 v[126:127], v[12:13], v[152:153], v[156:157]
	v_pk_fma_f32 v[128:129], v[14:15], v[176:177], v[180:181]
	v_fmac_f32_e32 v8, v116, v116
	v_fmac_f32_e32 v9, v114, v114
	v_add_f32_e32 v8, v8, v9
	v_mul_f32_e32 v9, v129, v129
	v_mul_f32_e32 v10, v127, v127
	v_fmac_f32_e32 v9, v128, v128
	v_fmac_f32_e32 v10, v126, v126
	v_add_f32_e32 v9, v9, v10
	v_add_f32_e32 v8, v8, v9
	v_add_f32_e32 v7, v7, v8
	v_mov_b32_e32 v8, v7
	s_nop 1
	v_permlane16_swap_b32 v8, v7
	s_nop 0
	s_waitcnt lgkmcnt(0)
	v_add_f32_e32 v7, v7, v8
	v_mov_b32_e32 v8, v7
	s_nop 1
	v_permlane32_swap_b32 v8, v7
	s_nop 0
	s_and_saveexec_b64 s[20:21], vcc
	s_cbranch_execz .LBB0_1488
	s_waitcnt lgkmcnt(0)
	v_add_f32_e32 v7, v7, v8
	ds_write_b32 v5, v7 offset:512
.LBB0_1488:
	s_or_b64 exec, exec, s[20:21]
	s_waitcnt lgkmcnt(0)
	s_waitcnt vmcnt(8)
	v_mov_b64_e32 v[8:9], v[232:233]
	v_mov_b64_e32 v[10:11], v[234:235]
	v_mov_b64_e32 v[12:13], v[236:237]
	v_mov_b64_e32 v[14:15], v[238:239]
	v_mov_b64_e32 v[150:151], v[240:241]
	v_mov_b64_e32 v[152:153], v[242:243]
	v_mov_b64_e32 v[154:155], v[244:245]
	v_mov_b64_e32 v[156:157], v[246:247]
	v_lshl_add_u64 v[254:255], v[254:255], 0, v[250:251]
	v_lshl_add_u64 v[196:197], v[196:197], 0, v[250:251]
	global_load_dwordx4 v[232:235], v[254:255], off
	global_load_dwordx4 v[236:239], v[196:197], off
	global_load_dwordx4 v[240:243], v[254:255], off offset:256
	global_load_dwordx4 v[244:247], v[196:197], off offset:256
	v_pk_mul_f32 v[16:17], v[112:113], s[6:7] op_sel_hi:[1,0]
	v_pk_mul_f32 v[110:111], v[110:111], s[6:7] op_sel_hi:[1,0]
	v_pk_mul_f32 v[108:109], v[108:109], s[6:7] op_sel_hi:[1,0]
	v_pk_mul_f32 v[106:107], v[106:107], s[6:7] op_sel_hi:[1,0]
	v_pk_mul_f32 v[104:105], v[104:105], s[6:7] op_sel_hi:[1,0]
	v_pk_mul_f32 v[110:111], v[110:111], s[2:3] op_sel_hi:[1,0]
	v_pk_mul_f32 v[16:17], v[16:17], s[2:3] op_sel_hi:[1,0]
	v_pk_mul_f32 v[106:107], v[106:107], s[2:3] op_sel_hi:[1,0]
	v_pk_mul_f32 v[108:109], v[108:109], s[2:3] op_sel_hi:[1,0]
	v_pk_mul_f32 v[112:113], v[104:105], s[2:3] op_sel_hi:[1,0]
	v_exp_f32_e32 v104, v110
	v_exp_f32_e32 v105, v111
	v_exp_f32_e32 v16, v16
	v_exp_f32_e32 v17, v17
	v_exp_f32_e32 v106, v106
	v_exp_f32_e32 v107, v107
	v_exp_f32_e32 v108, v108
	v_exp_f32_e32 v109, v109
	v_pk_mul_f32 v[102:103], v[102:103], s[6:7] op_sel_hi:[1,0]
	v_pk_add_f32 v[16:17], v[16:17], 1.0 op_sel_hi:[1,0]
	v_pk_mul_f32 v[102:103], v[102:103], s[2:3] op_sel_hi:[1,0]
	v_rcp_f32_e32 v16, v16
	v_exp_f32_e32 v110, v102
	v_exp_f32_e32 v111, v103
	v_pk_add_f32 v[102:103], v[104:105], 1.0 op_sel_hi:[1,0]
	v_pk_add_f32 v[104:105], v[106:107], 1.0 op_sel_hi:[1,0]
	v_pk_add_f32 v[106:107], v[108:109], 1.0 op_sel_hi:[1,0]
	v_rcp_f32_e32 v102, v102
	v_rcp_f32_e32 v103, v103
	v_rcp_f32_e32 v17, v17
	v_rcp_f32_e32 v104, v104
	v_rcp_f32_e32 v105, v105
	v_rcp_f32_e32 v158, v106
	v_rcp_f32_e32 v159, v107
	v_lshlrev_b32_e32 v170, 16, v12
	v_lshlrev_b32_e32 v108, 16, v8
	v_and_b32_e32 v109, 0xffff0000, v8
	v_lshlrev_b32_e32 v8, 16, v9
	v_and_b32_e32 v9, 0xffff0000, v9
	v_lshlrev_b32_e32 v160, 16, v10
	v_and_b32_e32 v161, 0xffff0000, v10
	v_lshlrev_b32_e32 v10, 16, v11
	v_and_b32_e32 v11, 0xffff0000, v11
	v_and_b32_e32 v171, 0xffff0000, v12
	v_lshlrev_b32_e32 v12, 16, v13
	v_and_b32_e32 v13, 0xffff0000, v13
	v_lshlrev_b32_e32 v172, 16, v14
	v_and_b32_e32 v173, 0xffff0000, v14
	v_lshlrev_b32_e32 v14, 16, v15
	v_and_b32_e32 v15, 0xffff0000, v15
	v_pk_fma_f32 v[106:107], v[16:17], v[8:9], v[12:13]
	v_pk_fma_f32 v[108:109], v[102:103], v[108:109], v[170:171]
	v_pk_fma_f32 v[102:103], v[158:159], v[10:11], v[14:15]
	v_pk_fma_f32 v[104:105], v[104:105], v[160:161], v[172:173]
	v_mul_f32_e32 v7, v109, v109
	v_mul_f32_e32 v8, v107, v107
	v_mul_f32_e32 v9, v105, v105
	v_mul_f32_e32 v10, v103, v103
	v_fmac_f32_e32 v7, v108, v108
	v_fmac_f32_e32 v8, v106, v106
	v_fmac_f32_e32 v9, v104, v104
	v_fmac_f32_e32 v10, v102, v102
	v_add_f32_e32 v7, v7, v8
	v_add_f32_e32 v8, v9, v10
	v_add_f32_e32 v7, v7, v8
	v_exp_f32_e32 v8, v112
	v_exp_f32_e32 v9, v113
	v_pk_mul_f32 v[12:13], v[100:101], s[6:7] op_sel_hi:[1,0]
	v_pk_mul_f32 v[14:15], v[98:99], s[6:7] op_sel_hi:[1,0]
	v_pk_mul_f32 v[12:13], v[12:13], s[2:3] op_sel_hi:[1,0]
	v_pk_mul_f32 v[14:15], v[14:15], s[2:3] op_sel_hi:[1,0]
	v_exp_f32_e32 v12, v12
	v_exp_f32_e32 v14, v14
	v_exp_f32_e32 v15, v15
	v_exp_f32_e32 v13, v13
	v_pk_add_f32 v[10:11], v[110:111], 1.0 op_sel_hi:[1,0]
	v_pk_add_f32 v[8:9], v[8:9], 1.0 op_sel_hi:[1,0]
	v_rcp_f32_e32 v10, v10
	v_rcp_f32_e32 v11, v11
	v_rcp_f32_e32 v8, v8
	v_rcp_f32_e32 v9, v9
	v_pk_add_f32 v[14:15], v[14:15], 1.0 op_sel_hi:[1,0]
	v_pk_add_f32 v[12:13], v[12:13], 1.0 op_sel_hi:[1,0]
	v_rcp_f32_e32 v14, v14
	v_rcp_f32_e32 v12, v12
	v_rcp_f32_e32 v13, v13
	v_rcp_f32_e32 v15, v15
	v_lshlrev_b32_e32 v174, 16, v150
	v_and_b32_e32 v175, 0xffff0000, v150
	v_lshlrev_b32_e32 v150, 16, v151
	v_and_b32_e32 v151, 0xffff0000, v151
	v_lshlrev_b32_e32 v178, 16, v154
	v_and_b32_e32 v179, 0xffff0000, v154
	v_lshlrev_b32_e32 v154, 16, v155
	v_and_b32_e32 v155, 0xffff0000, v155
	v_pk_fma_f32 v[100:101], v[8:9], v[150:151], v[154:155]
	v_pk_fma_f32 v[110:111], v[10:11], v[174:175], v[178:179]
	v_lshlrev_b32_e32 v176, 16, v152
	v_and_b32_e32 v177, 0xffff0000, v152
	v_lshlrev_b32_e32 v152, 16, v153
	v_and_b32_e32 v153, 0xffff0000, v153
	v_lshlrev_b32_e32 v180, 16, v156
	v_and_b32_e32 v181, 0xffff0000, v156
	v_lshlrev_b32_e32 v156, 16, v157
	v_and_b32_e32 v157, 0xffff0000, v157
	v_mul_f32_e32 v8, v111, v111
	v_mul_f32_e32 v9, v101, v101
	v_pk_fma_f32 v[98:99], v[12:13], v[152:153], v[156:157]
	v_pk_fma_f32 v[112:113], v[14:15], v[176:177], v[180:181]
	v_fmac_f32_e32 v8, v110, v110
	v_fmac_f32_e32 v9, v100, v100
	v_add_f32_e32 v8, v8, v9
	v_mul_f32_e32 v9, v113, v113
	v_mul_f32_e32 v10, v99, v99
	v_fmac_f32_e32 v9, v112, v112
	v_fmac_f32_e32 v10, v98, v98
	v_add_f32_e32 v9, v9, v10
	v_add_f32_e32 v8, v8, v9
	v_add_f32_e32 v7, v7, v8
	v_mov_b32_e32 v8, v7
	s_nop 1
	v_permlane16_swap_b32 v8, v7
	s_nop 0
	s_waitcnt lgkmcnt(0)
	v_add_f32_e32 v7, v7, v8
	v_mov_b32_e32 v8, v7
	s_nop 1
	v_permlane32_swap_b32 v8, v7
	s_nop 0
	s_and_saveexec_b64 s[2:3], vcc
	s_cbranch_execz .LBB0_1490
	s_waitcnt lgkmcnt(0)
	v_add_f32_e32 v7, v7, v8
	ds_write_b32 v5, v7 offset:768
.LBB0_1490:
	s_or_b64 exec, exec, s[2:3]
	s_waitcnt lgkmcnt(0)
	s_waitcnt vmcnt(8)
	v_mov_b64_e32 v[8:9], v[200:201]
	v_mov_b64_e32 v[10:11], v[202:203]
	v_mov_b64_e32 v[12:13], v[204:205]
	v_mov_b64_e32 v[14:15], v[206:207]
	v_mov_b64_e32 v[150:151], v[208:209]
	v_mov_b64_e32 v[152:153], v[210:211]
	v_mov_b64_e32 v[154:155], v[212:213]
	v_mov_b64_e32 v[156:157], v[214:215]
	v_lshl_add_u64 v[254:255], v[254:255], 0, v[250:251]
	v_lshl_add_u64 v[196:197], v[196:197], 0, v[250:251]
	global_load_dwordx4 v[200:203], v[254:255], off
	global_load_dwordx4 v[204:207], v[196:197], off
	global_load_dwordx4 v[208:211], v[254:255], off offset:256
	global_load_dwordx4 v[212:215], v[196:197], off offset:256
	s_mov_b32 s2, 0xbfb8aa3b
	v_pk_mul_f32 v[16:17], v[96:97], s[6:7] op_sel_hi:[1,0]
	v_pk_mul_f32 v[94:95], v[94:95], s[6:7] op_sel_hi:[1,0]
	v_pk_mul_f32 v[92:93], v[92:93], s[6:7] op_sel_hi:[1,0]
	v_pk_mul_f32 v[90:91], v[90:91], s[6:7] op_sel_hi:[1,0]
	v_pk_mul_f32 v[96:97], v[88:89], s[6:7] op_sel_hi:[1,0]
	v_pk_mul_f32 v[86:87], v[86:87], s[6:7] op_sel_hi:[1,0]
	v_pk_mul_f32 v[88:89], v[94:95], s[2:3] op_sel_hi:[1,0]
	v_pk_mul_f32 v[16:17], v[16:17], s[2:3] op_sel_hi:[1,0]
	v_pk_mul_f32 v[90:91], v[90:91], s[2:3] op_sel_hi:[1,0]
	v_pk_mul_f32 v[92:93], v[92:93], s[2:3] op_sel_hi:[1,0]
	v_pk_mul_f32 v[94:95], v[86:87], s[2:3] op_sel_hi:[1,0]
	v_exp_f32_e32 v86, v88
	v_exp_f32_e32 v87, v89
	v_exp_f32_e32 v16, v16
	v_exp_f32_e32 v17, v17
	v_exp_f32_e32 v88, v90
	v_exp_f32_e32 v89, v91
	v_exp_f32_e32 v90, v92
	v_exp_f32_e32 v91, v93
	v_pk_add_f32 v[86:87], v[86:87], 1.0 op_sel_hi:[1,0]
	v_pk_add_f32 v[16:17], v[16:17], 1.0 op_sel_hi:[1,0]
	v_pk_add_f32 v[88:89], v[88:89], 1.0 op_sel_hi:[1,0]
	v_pk_add_f32 v[90:91], v[90:91], 1.0 op_sel_hi:[1,0]
	v_rcp_f32_e32 v86, v86
	v_rcp_f32_e32 v87, v87
	v_rcp_f32_e32 v16, v16
	v_rcp_f32_e32 v17, v17
	v_rcp_f32_e32 v88, v88
	v_rcp_f32_e32 v89, v89
	v_rcp_f32_e32 v158, v90
	v_rcp_f32_e32 v159, v91
	v_add_u32_e32 v19, 0x80, v189
	v_lshlrev_b32_e32 v170, 16, v12
	v_lshlrev_b32_e32 v92, 16, v8
	v_and_b32_e32 v93, 0xffff0000, v8
	v_lshlrev_b32_e32 v8, 16, v9
	v_and_b32_e32 v9, 0xffff0000, v9
	v_lshlrev_b32_e32 v160, 16, v10
	v_and_b32_e32 v161, 0xffff0000, v10
	v_lshlrev_b32_e32 v10, 16, v11
	v_and_b32_e32 v11, 0xffff0000, v11
	v_and_b32_e32 v171, 0xffff0000, v12
	v_lshlrev_b32_e32 v12, 16, v13
	v_and_b32_e32 v13, 0xffff0000, v13
	v_lshlrev_b32_e32 v172, 16, v14
	v_and_b32_e32 v173, 0xffff0000, v14
	v_lshlrev_b32_e32 v14, 16, v15
	v_and_b32_e32 v15, 0xffff0000, v15
	v_pk_fma_f32 v[90:91], v[16:17], v[8:9], v[12:13]
	v_pk_fma_f32 v[92:93], v[86:87], v[92:93], v[170:171]
	v_pk_fma_f32 v[86:87], v[158:159], v[10:11], v[14:15]
	v_pk_fma_f32 v[88:89], v[88:89], v[160:161], v[172:173]
	v_mul_f32_e32 v7, v93, v93
	v_mul_f32_e32 v8, v91, v91
	v_mul_f32_e32 v9, v89, v89
	v_mul_f32_e32 v10, v87, v87
	v_fmac_f32_e32 v7, v92, v92
	v_fmac_f32_e32 v8, v90, v90
	v_fmac_f32_e32 v9, v88, v88
	v_fmac_f32_e32 v10, v86, v86
	v_add_f32_e32 v7, v7, v8
	v_add_f32_e32 v8, v9, v10
	v_pk_mul_f32 v[10:11], v[96:97], s[2:3] op_sel_hi:[1,0]
	v_add_f32_e32 v7, v7, v8
	v_exp_f32_e32 v8, v94
	v_exp_f32_e32 v9, v95
	v_exp_f32_e32 v10, v10
	v_exp_f32_e32 v11, v11
	v_pk_mul_f32 v[12:13], v[84:85], s[6:7] op_sel_hi:[1,0]
	v_pk_mul_f32 v[14:15], v[82:83], s[6:7] op_sel_hi:[1,0]
	v_pk_mul_f32 v[12:13], v[12:13], s[2:3] op_sel_hi:[1,0]
	v_pk_mul_f32 v[14:15], v[14:15], s[2:3] op_sel_hi:[1,0]
	v_exp_f32_e32 v12, v12
	v_exp_f32_e32 v14, v14
	v_exp_f32_e32 v15, v15
	v_exp_f32_e32 v13, v13
	v_pk_add_f32 v[8:9], v[8:9], 1.0 op_sel_hi:[1,0]
	v_pk_add_f32 v[10:11], v[10:11], 1.0 op_sel_hi:[1,0]
	v_rcp_f32_e32 v8, v8
	v_rcp_f32_e32 v9, v9
	v_rcp_f32_e32 v10, v10
	v_rcp_f32_e32 v11, v11
	v_pk_add_f32 v[14:15], v[14:15], 1.0 op_sel_hi:[1,0]
	v_pk_add_f32 v[12:13], v[12:13], 1.0 op_sel_hi:[1,0]
	v_rcp_f32_e32 v14, v14
	v_rcp_f32_e32 v12, v12
	v_rcp_f32_e32 v13, v13
	v_rcp_f32_e32 v15, v15
	v_lshlrev_b32_e32 v174, 16, v150
	v_and_b32_e32 v175, 0xffff0000, v150
	v_lshlrev_b32_e32 v150, 16, v151
	v_and_b32_e32 v151, 0xffff0000, v151
	v_lshlrev_b32_e32 v178, 16, v154
	v_and_b32_e32 v179, 0xffff0000, v154
	v_lshlrev_b32_e32 v154, 16, v155
	v_and_b32_e32 v155, 0xffff0000, v155
	v_pk_fma_f32 v[84:85], v[10:11], v[150:151], v[154:155]
	v_pk_fma_f32 v[94:95], v[8:9], v[174:175], v[178:179]
	v_lshlrev_b32_e32 v176, 16, v152
	v_and_b32_e32 v177, 0xffff0000, v152
	v_lshlrev_b32_e32 v152, 16, v153
	v_and_b32_e32 v153, 0xffff0000, v153
	v_lshlrev_b32_e32 v180, 16, v156
	v_and_b32_e32 v181, 0xffff0000, v156
	v_lshlrev_b32_e32 v156, 16, v157
	v_and_b32_e32 v157, 0xffff0000, v157
	v_mul_f32_e32 v8, v95, v95
	v_mul_f32_e32 v9, v85, v85
	v_pk_fma_f32 v[82:83], v[12:13], v[152:153], v[156:157]
	v_pk_fma_f32 v[96:97], v[14:15], v[176:177], v[180:181]
	v_fmac_f32_e32 v8, v94, v94
	v_fmac_f32_e32 v9, v84, v84
	v_add_f32_e32 v8, v8, v9
	v_mul_f32_e32 v9, v97, v97
	v_mul_f32_e32 v10, v83, v83
	v_fmac_f32_e32 v9, v96, v96
	v_fmac_f32_e32 v10, v82, v82
	v_add_f32_e32 v9, v9, v10
	v_add_f32_e32 v8, v8, v9
	v_add_f32_e32 v7, v7, v8
	v_mov_b32_e32 v8, v7
	s_nop 1
	v_permlane16_swap_b32 v8, v7
	s_nop 0
	s_waitcnt lgkmcnt(0)
	v_add_f32_e32 v7, v7, v8
	v_mov_b32_e32 v8, v7
	s_nop 1
	v_permlane32_swap_b32 v8, v7
	s_nop 0
	s_and_saveexec_b64 s[20:21], vcc
	s_cbranch_execz .LBB0_1492
	v_lshl_add_u32 v9, v19, 4, s5
	s_waitcnt lgkmcnt(0)
	v_add_f32_e32 v7, v7, v8
	ds_write_b32 v9, v7
.LBB0_1492:
	s_or_b64 exec, exec, s[20:21]
	v_add_u32_e32 v150, 0x90, v18
	v_ashrrev_i32_e32 v151, 31, v150
	s_waitcnt lgkmcnt(0)
	s_waitcnt vmcnt(8)
	v_mov_b64_e32 v[8:9], v[216:217]
	v_mov_b64_e32 v[10:11], v[218:219]
	v_mov_b64_e32 v[12:13], v[220:221]
	v_mov_b64_e32 v[14:15], v[222:223]
	v_mov_b64_e32 v[152:153], v[224:225]
	v_mov_b64_e32 v[154:155], v[226:227]
	v_mov_b64_e32 v[156:157], v[228:229]
	v_mov_b64_e32 v[158:159], v[230:231]
	v_pk_mul_f32 v[16:17], v[80:81], s[6:7] op_sel_hi:[1,0]
	v_pk_mul_f32 v[78:79], v[78:79], s[6:7] op_sel_hi:[1,0]
	v_pk_mul_f32 v[76:77], v[76:77], s[6:7] op_sel_hi:[1,0]
	v_pk_mul_f32 v[74:75], v[74:75], s[6:7] op_sel_hi:[1,0]
	v_pk_mul_f32 v[72:73], v[72:73], s[6:7] op_sel_hi:[1,0]
	v_pk_mul_f32 v[78:79], v[78:79], s[2:3] op_sel_hi:[1,0]
	v_pk_mul_f32 v[16:17], v[16:17], s[2:3] op_sel_hi:[1,0]
	v_pk_mul_f32 v[74:75], v[74:75], s[2:3] op_sel_hi:[1,0]
	v_pk_mul_f32 v[76:77], v[76:77], s[2:3] op_sel_hi:[1,0]
	v_pk_mul_f32 v[80:81], v[72:73], s[2:3] op_sel_hi:[1,0]
	v_exp_f32_e32 v72, v78
	v_exp_f32_e32 v73, v79
	v_exp_f32_e32 v16, v16
	v_exp_f32_e32 v17, v17
	v_exp_f32_e32 v74, v74
	v_exp_f32_e32 v75, v75
	v_exp_f32_e32 v76, v76
	v_exp_f32_e32 v77, v77
	v_pk_mul_f32 v[70:71], v[70:71], s[6:7] op_sel_hi:[1,0]
	v_pk_add_f32 v[16:17], v[16:17], 1.0 op_sel_hi:[1,0]
	v_pk_mul_f32 v[70:71], v[70:71], s[2:3] op_sel_hi:[1,0]
	v_rcp_f32_e32 v16, v16
	v_exp_f32_e32 v78, v70
	v_exp_f32_e32 v79, v71
	v_pk_add_f32 v[70:71], v[72:73], 1.0 op_sel_hi:[1,0]
	v_pk_add_f32 v[72:73], v[74:75], 1.0 op_sel_hi:[1,0]
	v_pk_add_f32 v[74:75], v[76:77], 1.0 op_sel_hi:[1,0]
	v_rcp_f32_e32 v70, v70
	v_rcp_f32_e32 v71, v71
	v_rcp_f32_e32 v17, v17
	v_rcp_f32_e32 v72, v72
	v_rcp_f32_e32 v73, v73
	v_rcp_f32_e32 v160, v74
	v_rcp_f32_e32 v161, v75
	v_lshlrev_b32_e32 v172, 16, v12
	v_lshlrev_b32_e32 v76, 16, v8
	v_and_b32_e32 v77, 0xffff0000, v8
	v_lshlrev_b32_e32 v8, 16, v9
	v_and_b32_e32 v9, 0xffff0000, v9
	v_lshlrev_b32_e32 v170, 16, v10
	v_and_b32_e32 v171, 0xffff0000, v10
	v_lshlrev_b32_e32 v10, 16, v11
	v_and_b32_e32 v11, 0xffff0000, v11
	v_and_b32_e32 v173, 0xffff0000, v12
	v_lshlrev_b32_e32 v12, 16, v13
	v_and_b32_e32 v13, 0xffff0000, v13
	v_lshlrev_b32_e32 v174, 16, v14
	v_and_b32_e32 v175, 0xffff0000, v14
	v_lshlrev_b32_e32 v14, 16, v15
	v_and_b32_e32 v15, 0xffff0000, v15
	v_pk_fma_f32 v[74:75], v[16:17], v[8:9], v[12:13]
	v_pk_fma_f32 v[76:77], v[70:71], v[76:77], v[172:173]
	v_pk_fma_f32 v[70:71], v[160:161], v[10:11], v[14:15]
	v_pk_fma_f32 v[72:73], v[72:73], v[170:171], v[174:175]
	v_mul_f32_e32 v7, v77, v77
	v_mul_f32_e32 v8, v75, v75
	v_mul_f32_e32 v9, v73, v73
	v_mul_f32_e32 v10, v71, v71
	v_fmac_f32_e32 v7, v76, v76
	v_fmac_f32_e32 v8, v74, v74
	v_fmac_f32_e32 v9, v72, v72
	v_fmac_f32_e32 v10, v70, v70
	v_add_f32_e32 v7, v7, v8
	v_add_f32_e32 v8, v9, v10
	v_add_f32_e32 v7, v7, v8
	v_exp_f32_e32 v8, v80
	v_exp_f32_e32 v9, v81
	v_pk_mul_f32 v[12:13], v[68:69], s[6:7] op_sel_hi:[1,0]
	v_pk_mul_f32 v[14:15], v[66:67], s[6:7] op_sel_hi:[1,0]
	v_pk_mul_f32 v[12:13], v[12:13], s[2:3] op_sel_hi:[1,0]
	v_pk_mul_f32 v[14:15], v[14:15], s[2:3] op_sel_hi:[1,0]
	v_exp_f32_e32 v12, v12
	v_exp_f32_e32 v14, v14
	v_exp_f32_e32 v15, v15
	v_exp_f32_e32 v13, v13
	v_pk_add_f32 v[10:11], v[78:79], 1.0 op_sel_hi:[1,0]
	v_pk_add_f32 v[8:9], v[8:9], 1.0 op_sel_hi:[1,0]
	v_rcp_f32_e32 v10, v10
	v_rcp_f32_e32 v11, v11
	v_rcp_f32_e32 v8, v8
	v_rcp_f32_e32 v9, v9
	v_pk_add_f32 v[14:15], v[14:15], 1.0 op_sel_hi:[1,0]
	v_pk_add_f32 v[12:13], v[12:13], 1.0 op_sel_hi:[1,0]
	v_rcp_f32_e32 v14, v14
	v_rcp_f32_e32 v12, v12
	v_rcp_f32_e32 v13, v13
	v_rcp_f32_e32 v15, v15
	v_lshlrev_b32_e32 v176, 16, v152
	v_and_b32_e32 v177, 0xffff0000, v152
	v_lshlrev_b32_e32 v152, 16, v153
	v_and_b32_e32 v153, 0xffff0000, v153
	v_lshlrev_b32_e32 v180, 16, v156
	v_and_b32_e32 v181, 0xffff0000, v156
	v_lshlrev_b32_e32 v156, 16, v157
	v_and_b32_e32 v157, 0xffff0000, v157
	v_pk_fma_f32 v[68:69], v[8:9], v[152:153], v[156:157]
	v_pk_fma_f32 v[78:79], v[10:11], v[176:177], v[180:181]
	v_lshlrev_b32_e32 v178, 16, v154
	v_and_b32_e32 v179, 0xffff0000, v154
	v_lshlrev_b32_e32 v154, 16, v155
	v_and_b32_e32 v155, 0xffff0000, v155
	v_lshlrev_b32_e32 v190, 16, v158
	v_and_b32_e32 v191, 0xffff0000, v158
	v_lshlrev_b32_e32 v158, 16, v159
	v_and_b32_e32 v159, 0xffff0000, v159
	v_mul_f32_e32 v8, v79, v79
	v_mul_f32_e32 v9, v69, v69
	v_pk_fma_f32 v[66:67], v[12:13], v[154:155], v[158:159]
	v_pk_fma_f32 v[80:81], v[14:15], v[178:179], v[190:191]
	v_fmac_f32_e32 v8, v78, v78
	v_fmac_f32_e32 v9, v68, v68
	v_add_f32_e32 v8, v8, v9
	v_mul_f32_e32 v9, v81, v81
	v_mul_f32_e32 v10, v67, v67
	v_fmac_f32_e32 v9, v80, v80
	v_fmac_f32_e32 v10, v66, v66
	v_add_f32_e32 v9, v9, v10
	v_add_f32_e32 v8, v8, v9
	v_add_f32_e32 v7, v7, v8
	v_mov_b32_e32 v8, v7
	s_nop 1
	v_permlane16_swap_b32 v8, v7
	s_nop 0
	s_waitcnt lgkmcnt(0)
	v_add_f32_e32 v7, v7, v8
	v_mov_b32_e32 v8, v7
	s_nop 1
	v_permlane32_swap_b32 v8, v7
	s_nop 0
	s_and_saveexec_b64 s[2:3], vcc
	s_cbranch_execz .LBB0_1494
	s_waitcnt lgkmcnt(0)
	v_add_f32_e32 v7, v7, v8
	ds_write_b32 v5, v7 offset:2304
.LBB0_1494:
	s_or_b64 exec, exec, s[2:3]
	v_add_u32_e32 v152, 0xa0, v18
	v_ashrrev_i32_e32 v153, 31, v152
	s_waitcnt lgkmcnt(0)
	s_waitcnt vmcnt(4)
	v_mov_b64_e32 v[8:9], v[232:233]
	v_mov_b64_e32 v[10:11], v[234:235]
	v_mov_b64_e32 v[12:13], v[236:237]
	v_mov_b64_e32 v[14:15], v[238:239]
	v_mov_b64_e32 v[154:155], v[240:241]
	v_mov_b64_e32 v[156:157], v[242:243]
	v_mov_b64_e32 v[158:159], v[244:245]
	v_mov_b64_e32 v[160:161], v[246:247]
	s_mov_b32 s2, 0xbfb8aa3b
	v_pk_mul_f32 v[16:17], v[64:65], s[6:7] op_sel_hi:[1,0]
	v_pk_mul_f32 v[62:63], v[62:63], s[6:7] op_sel_hi:[1,0]
	v_pk_mul_f32 v[60:61], v[60:61], s[6:7] op_sel_hi:[1,0]
	v_pk_mul_f32 v[58:59], v[58:59], s[6:7] op_sel_hi:[1,0]
	v_pk_mul_f32 v[64:65], v[56:57], s[6:7] op_sel_hi:[1,0]
	v_pk_mul_f32 v[54:55], v[54:55], s[6:7] op_sel_hi:[1,0]
	v_pk_mul_f32 v[56:57], v[62:63], s[2:3] op_sel_hi:[1,0]
	v_pk_mul_f32 v[16:17], v[16:17], s[2:3] op_sel_hi:[1,0]
	v_pk_mul_f32 v[58:59], v[58:59], s[2:3] op_sel_hi:[1,0]
	v_pk_mul_f32 v[60:61], v[60:61], s[2:3] op_sel_hi:[1,0]
	v_pk_mul_f32 v[62:63], v[54:55], s[2:3] op_sel_hi:[1,0]
	v_exp_f32_e32 v54, v56
	v_exp_f32_e32 v55, v57
	v_exp_f32_e32 v16, v16
	v_exp_f32_e32 v17, v17
	v_exp_f32_e32 v56, v58
	v_exp_f32_e32 v57, v59
	v_exp_f32_e32 v58, v60
	v_exp_f32_e32 v59, v61
	v_pk_add_f32 v[54:55], v[54:55], 1.0 op_sel_hi:[1,0]
	v_pk_add_f32 v[16:17], v[16:17], 1.0 op_sel_hi:[1,0]
	v_pk_add_f32 v[56:57], v[56:57], 1.0 op_sel_hi:[1,0]
	v_pk_add_f32 v[58:59], v[58:59], 1.0 op_sel_hi:[1,0]
	v_rcp_f32_e32 v54, v54
	v_rcp_f32_e32 v55, v55
	v_rcp_f32_e32 v16, v16
	v_rcp_f32_e32 v17, v17
	v_rcp_f32_e32 v56, v56
	v_rcp_f32_e32 v57, v57
	v_rcp_f32_e32 v170, v58
	v_rcp_f32_e32 v171, v59
	v_exp_f32_e32 v62, v62
	v_exp_f32_e32 v63, v63
	v_lshlrev_b32_e32 v174, 16, v12
	v_lshlrev_b32_e32 v60, 16, v8
	v_and_b32_e32 v61, 0xffff0000, v8
	v_lshlrev_b32_e32 v8, 16, v9
	v_and_b32_e32 v9, 0xffff0000, v9
	v_lshlrev_b32_e32 v172, 16, v10
	v_and_b32_e32 v173, 0xffff0000, v10
	v_lshlrev_b32_e32 v10, 16, v11
	v_and_b32_e32 v11, 0xffff0000, v11
	v_and_b32_e32 v175, 0xffff0000, v12
	v_lshlrev_b32_e32 v12, 16, v13
	v_and_b32_e32 v13, 0xffff0000, v13
	v_lshlrev_b32_e32 v176, 16, v14
	v_and_b32_e32 v177, 0xffff0000, v14
	v_lshlrev_b32_e32 v14, 16, v15
	v_and_b32_e32 v15, 0xffff0000, v15
	v_pk_fma_f32 v[58:59], v[16:17], v[8:9], v[12:13]
	v_pk_fma_f32 v[60:61], v[54:55], v[60:61], v[174:175]
	v_pk_fma_f32 v[54:55], v[170:171], v[10:11], v[14:15]
	v_pk_fma_f32 v[56:57], v[56:57], v[172:173], v[176:177]
	v_mul_f32_e32 v7, v61, v61
	v_mul_f32_e32 v8, v59, v59
	v_mul_f32_e32 v9, v57, v57
	v_mul_f32_e32 v10, v55, v55
	v_fmac_f32_e32 v7, v60, v60
	v_fmac_f32_e32 v8, v58, v58
	v_fmac_f32_e32 v9, v56, v56
	v_fmac_f32_e32 v10, v54, v54
	v_add_f32_e32 v7, v7, v8
	v_add_f32_e32 v8, v9, v10
	v_add_f32_e32 v7, v7, v8
	v_pk_mul_f32 v[8:9], v[64:65], s[2:3] op_sel_hi:[1,0]
	v_pk_mul_f32 v[12:13], v[52:53], s[6:7] op_sel_hi:[1,0]
	v_exp_f32_e32 v8, v8
	v_exp_f32_e32 v9, v9
	v_pk_mul_f32 v[14:15], v[50:51], s[6:7] op_sel_hi:[1,0]
	v_pk_mul_f32 v[12:13], v[12:13], s[2:3] op_sel_hi:[1,0]
	v_pk_mul_f32 v[14:15], v[14:15], s[2:3] op_sel_hi:[1,0]
	v_exp_f32_e32 v12, v12
	v_exp_f32_e32 v14, v14
	v_exp_f32_e32 v15, v15
	v_exp_f32_e32 v13, v13
	v_pk_add_f32 v[10:11], v[62:63], 1.0 op_sel_hi:[1,0]
	v_pk_add_f32 v[8:9], v[8:9], 1.0 op_sel_hi:[1,0]
	v_rcp_f32_e32 v10, v10
	v_rcp_f32_e32 v11, v11
	v_rcp_f32_e32 v8, v8
	v_rcp_f32_e32 v9, v9
	v_pk_add_f32 v[14:15], v[14:15], 1.0 op_sel_hi:[1,0]
	v_pk_add_f32 v[12:13], v[12:13], 1.0 op_sel_hi:[1,0]
	v_rcp_f32_e32 v14, v14
	v_rcp_f32_e32 v12, v12
	v_rcp_f32_e32 v13, v13
	v_rcp_f32_e32 v15, v15
	v_lshlrev_b32_e32 v178, 16, v154
	v_and_b32_e32 v179, 0xffff0000, v154
	v_lshlrev_b32_e32 v154, 16, v155
	v_and_b32_e32 v155, 0xffff0000, v155
	v_lshlrev_b32_e32 v190, 16, v158
	v_and_b32_e32 v191, 0xffff0000, v158
	v_lshlrev_b32_e32 v158, 16, v159
	v_and_b32_e32 v159, 0xffff0000, v159
	v_pk_fma_f32 v[52:53], v[8:9], v[154:155], v[158:159]
	v_pk_fma_f32 v[62:63], v[10:11], v[178:179], v[190:191]
	v_lshlrev_b32_e32 v180, 16, v156
	v_and_b32_e32 v181, 0xffff0000, v156
	v_lshlrev_b32_e32 v156, 16, v157
	v_and_b32_e32 v157, 0xffff0000, v157
	v_lshlrev_b32_e32 v192, 16, v160
	v_and_b32_e32 v193, 0xffff0000, v160
	v_lshlrev_b32_e32 v160, 16, v161
	v_and_b32_e32 v161, 0xffff0000, v161
	v_mul_f32_e32 v8, v63, v63
	v_mul_f32_e32 v9, v53, v53
	v_pk_fma_f32 v[50:51], v[12:13], v[156:157], v[160:161]
	v_pk_fma_f32 v[64:65], v[14:15], v[180:181], v[192:193]
	v_fmac_f32_e32 v8, v62, v62
	v_fmac_f32_e32 v9, v52, v52
	v_add_f32_e32 v8, v8, v9
	v_mul_f32_e32 v9, v65, v65
	v_mul_f32_e32 v10, v51, v51
	v_fmac_f32_e32 v9, v64, v64
	v_fmac_f32_e32 v10, v50, v50
	v_add_f32_e32 v9, v9, v10
	v_add_f32_e32 v8, v8, v9
	v_add_f32_e32 v7, v7, v8
	v_mov_b32_e32 v8, v7
	s_nop 1
	v_permlane16_swap_b32 v8, v7
	s_nop 0
	s_waitcnt lgkmcnt(0)
	v_add_f32_e32 v7, v7, v8
	v_mov_b32_e32 v8, v7
	s_nop 1
	v_permlane32_swap_b32 v8, v7
	s_nop 0
	s_and_saveexec_b64 s[20:21], vcc
	s_cbranch_execz .LBB0_1496
	s_waitcnt lgkmcnt(0)
	v_add_f32_e32 v7, v7, v8
	ds_write_b32 v5, v7 offset:2560
.LBB0_1496:
	s_or_b64 exec, exec, s[20:21]
	v_add_u32_e32 v154, 0xb0, v18
	v_ashrrev_i32_e32 v155, 31, v154
	s_waitcnt lgkmcnt(0)
	s_waitcnt vmcnt(0)
	v_mov_b64_e32 v[8:9], v[200:201]
	v_mov_b64_e32 v[10:11], v[202:203]
	v_mov_b64_e32 v[12:13], v[204:205]
	v_mov_b64_e32 v[14:15], v[206:207]
	v_mov_b64_e32 v[156:157], v[208:209]
	v_mov_b64_e32 v[158:159], v[210:211]
	v_mov_b64_e32 v[170:171], v[212:213]
	v_mov_b64_e32 v[172:173], v[214:215]
	v_pk_mul_f32 v[16:17], v[48:49], s[6:7] op_sel_hi:[1,0]
	v_pk_mul_f32 v[46:47], v[46:47], s[6:7] op_sel_hi:[1,0]
	v_pk_mul_f32 v[44:45], v[44:45], s[6:7] op_sel_hi:[1,0]
	v_pk_mul_f32 v[42:43], v[42:43], s[6:7] op_sel_hi:[1,0]
	v_pk_mul_f32 v[40:41], v[40:41], s[6:7] op_sel_hi:[1,0]
	v_pk_mul_f32 v[46:47], v[46:47], s[2:3] op_sel_hi:[1,0]
	v_pk_mul_f32 v[16:17], v[16:17], s[2:3] op_sel_hi:[1,0]
	v_pk_mul_f32 v[42:43], v[42:43], s[2:3] op_sel_hi:[1,0]
	v_pk_mul_f32 v[44:45], v[44:45], s[2:3] op_sel_hi:[1,0]
	v_pk_mul_f32 v[48:49], v[40:41], s[2:3] op_sel_hi:[1,0]
	v_exp_f32_e32 v40, v46
	v_exp_f32_e32 v41, v47
	v_exp_f32_e32 v16, v16
	v_exp_f32_e32 v17, v17
	v_exp_f32_e32 v42, v42
	v_exp_f32_e32 v43, v43
	v_exp_f32_e32 v44, v44
	v_exp_f32_e32 v45, v45
	v_pk_mul_f32 v[38:39], v[38:39], s[6:7] op_sel_hi:[1,0]
	v_pk_add_f32 v[16:17], v[16:17], 1.0 op_sel_hi:[1,0]
	v_pk_mul_f32 v[38:39], v[38:39], s[2:3] op_sel_hi:[1,0]
	v_rcp_f32_e32 v16, v16
	v_exp_f32_e32 v46, v38
	v_exp_f32_e32 v47, v39
	v_pk_add_f32 v[38:39], v[40:41], 1.0 op_sel_hi:[1,0]
	v_pk_add_f32 v[40:41], v[42:43], 1.0 op_sel_hi:[1,0]
	v_pk_add_f32 v[42:43], v[44:45], 1.0 op_sel_hi:[1,0]
	v_rcp_f32_e32 v38, v38
	v_rcp_f32_e32 v39, v39
	v_rcp_f32_e32 v17, v17
	v_rcp_f32_e32 v40, v40
	v_rcp_f32_e32 v41, v41
	v_rcp_f32_e32 v160, v42
	v_rcp_f32_e32 v161, v43
	v_lshlrev_b32_e32 v176, 16, v12
	v_lshlrev_b32_e32 v44, 16, v8
	v_and_b32_e32 v45, 0xffff0000, v8
	v_lshlrev_b32_e32 v8, 16, v9
	v_and_b32_e32 v9, 0xffff0000, v9
	v_lshlrev_b32_e32 v174, 16, v10
	v_and_b32_e32 v175, 0xffff0000, v10
	v_lshlrev_b32_e32 v10, 16, v11
	v_and_b32_e32 v11, 0xffff0000, v11
	v_and_b32_e32 v177, 0xffff0000, v12
	v_lshlrev_b32_e32 v12, 16, v13
	v_and_b32_e32 v13, 0xffff0000, v13
	v_lshlrev_b32_e32 v178, 16, v14
	v_and_b32_e32 v179, 0xffff0000, v14
	v_lshlrev_b32_e32 v14, 16, v15
	v_and_b32_e32 v15, 0xffff0000, v15
	v_pk_fma_f32 v[42:43], v[16:17], v[8:9], v[12:13]
	v_pk_fma_f32 v[44:45], v[38:39], v[44:45], v[176:177]
	v_pk_fma_f32 v[38:39], v[160:161], v[10:11], v[14:15]
	v_pk_fma_f32 v[40:41], v[40:41], v[174:175], v[178:179]
	v_mul_f32_e32 v7, v45, v45
	v_mul_f32_e32 v8, v43, v43
	v_mul_f32_e32 v9, v41, v41
	v_mul_f32_e32 v10, v39, v39
	v_fmac_f32_e32 v7, v44, v44
	v_fmac_f32_e32 v8, v42, v42
	v_fmac_f32_e32 v9, v40, v40
	v_fmac_f32_e32 v10, v38, v38
	v_add_f32_e32 v7, v7, v8
	v_add_f32_e32 v8, v9, v10
	v_add_f32_e32 v7, v7, v8
	v_exp_f32_e32 v8, v48
	v_exp_f32_e32 v9, v49
	v_pk_mul_f32 v[12:13], v[36:37], s[6:7] op_sel_hi:[1,0]
	v_pk_mul_f32 v[14:15], v[34:35], s[6:7] op_sel_hi:[1,0]
	v_pk_mul_f32 v[12:13], v[12:13], s[2:3] op_sel_hi:[1,0]
	v_pk_mul_f32 v[14:15], v[14:15], s[2:3] op_sel_hi:[1,0]
	v_exp_f32_e32 v12, v12
	v_exp_f32_e32 v14, v14
	v_exp_f32_e32 v15, v15
	v_exp_f32_e32 v13, v13
	v_pk_add_f32 v[10:11], v[46:47], 1.0 op_sel_hi:[1,0]
	v_pk_add_f32 v[8:9], v[8:9], 1.0 op_sel_hi:[1,0]
	v_rcp_f32_e32 v10, v10
	v_rcp_f32_e32 v11, v11
	v_rcp_f32_e32 v8, v8
	v_rcp_f32_e32 v9, v9
	v_pk_add_f32 v[14:15], v[14:15], 1.0 op_sel_hi:[1,0]
	v_pk_add_f32 v[12:13], v[12:13], 1.0 op_sel_hi:[1,0]
	v_rcp_f32_e32 v14, v14
	v_rcp_f32_e32 v12, v12
	v_rcp_f32_e32 v13, v13
	v_rcp_f32_e32 v15, v15
	v_lshlrev_b32_e32 v180, 16, v156
	v_and_b32_e32 v181, 0xffff0000, v156
	v_lshlrev_b32_e32 v156, 16, v157
	v_and_b32_e32 v157, 0xffff0000, v157
	v_lshlrev_b32_e32 v192, 16, v170
	v_and_b32_e32 v193, 0xffff0000, v170
	v_lshlrev_b32_e32 v170, 16, v171
	v_and_b32_e32 v171, 0xffff0000, v171
	v_pk_fma_f32 v[36:37], v[8:9], v[156:157], v[170:171]
	v_pk_fma_f32 v[46:47], v[10:11], v[180:181], v[192:193]
	v_lshlrev_b32_e32 v190, 16, v158
	v_and_b32_e32 v191, 0xffff0000, v158
	v_lshlrev_b32_e32 v158, 16, v159
	v_and_b32_e32 v159, 0xffff0000, v159
	v_lshlrev_b32_e32 v194, 16, v172
	v_and_b32_e32 v195, 0xffff0000, v172
	v_lshlrev_b32_e32 v172, 16, v173
	v_and_b32_e32 v173, 0xffff0000, v173
	v_mul_f32_e32 v8, v47, v47
	v_mul_f32_e32 v9, v37, v37
	v_pk_fma_f32 v[34:35], v[12:13], v[158:159], v[172:173]
	v_pk_fma_f32 v[48:49], v[14:15], v[190:191], v[194:195]
	v_fmac_f32_e32 v8, v46, v46
	v_fmac_f32_e32 v9, v36, v36
	v_add_f32_e32 v8, v8, v9
	v_mul_f32_e32 v9, v49, v49
	v_mul_f32_e32 v10, v35, v35
	v_fmac_f32_e32 v9, v48, v48
	v_fmac_f32_e32 v10, v34, v34
	v_add_f32_e32 v9, v9, v10
	v_add_f32_e32 v8, v8, v9
	v_add_f32_e32 v7, v7, v8
	v_mov_b32_e32 v4, v7
	s_nop 1
	v_permlane16_swap_b32 v4, v7
	s_nop 0
	s_waitcnt lgkmcnt(0)
	v_add_f32_e32 v4, v7, v4
	v_mov_b32_e32 v6, v4
	s_nop 1
	v_permlane32_swap_b32 v6, v4
	s_nop 0
	s_and_saveexec_b64 s[2:3], vcc
	s_cbranch_execz .LBB0_1498
	s_waitcnt lgkmcnt(0)
	v_add_f32_e32 v4, v4, v6
	ds_write_b32 v5, v4 offset:2816

.LBB0_1533:
	s_lshl_b32 s2, s5, 5
	s_lshl_b32 s1, s0, 8
	s_lshl_b32 s3, s4, 8
	s_or_b32 s2, s3, s2
	v_add_u32_e32 v18, s1, v189
	v_or_b32_e32 v2, s2, v1
	v_ashrrev_i32_e32 v19, 31, v18
	v_ashrrev_i32_e32 v3, 31, v2
	v_lshlrev_b64 v[4:5], 11, v[18:19]
	v_lshl_add_u64 v[20:21], v[4:5], 0, v[2:3]
	v_lshlrev_b64 v[8:9], 1, v[20:21]
	v_lshl_add_u64 v[12:13], s[18:19], 0, v[8:9]
	s_barrier
	global_load_dwordx4 v[4:7], v[12:13], off
	v_lshl_add_u64 v[16:17], s[16:17], 0, v[8:9]
	global_load_dwordx4 v[8:11], v[16:17], off
	s_nop 0
	global_load_dwordx4 v[12:15], v[12:13], off offset:256
	s_nop 0
	global_load_dwordx4 v[30:33], v[16:17], off offset:256
	v_lshlrev_b64 v[254:255], 11, v[18:19]
	v_lshl_add_u64 v[254:255], v[254:255], 0, v[2:3]
	v_lshlrev_b64 v[254:255], 1, v[254:255]
	v_mov_b32_e32 v250, 0x10000
	v_mov_b32_e32 v251, 0
	v_lshl_add_u64 v[196:197], s[16:17], 0, v[254:255]
	v_lshl_add_u64 v[254:255], s[18:19], 0, v[254:255]
	v_lshl_add_u64 v[254:255], v[254:255], 0, v[250:251]
	v_lshl_add_u64 v[196:197], v[196:197], 0, v[250:251]
	global_load_dwordx4 v[200:203], v[254:255], off
	global_load_dwordx4 v[204:207], v[196:197], off
	global_load_dwordx4 v[208:211], v[254:255], off offset:256
	global_load_dwordx4 v[212:215], v[196:197], off offset:256
	v_lshl_add_u64 v[254:255], v[254:255], 0, v[250:251]
	v_lshl_add_u64 v[196:197], v[196:197], 0, v[250:251]
	global_load_dwordx4 v[216:219], v[254:255], off
	global_load_dwordx4 v[220:223], v[196:197], off
	global_load_dwordx4 v[224:227], v[254:255], off offset:256
	global_load_dwordx4 v[228:231], v[196:197], off offset:256
	v_lshl_add_u64 v[254:255], v[254:255], 0, v[250:251]
	v_lshl_add_u64 v[196:197], v[196:197], 0, v[250:251]
	global_load_dwordx4 v[232:235], v[254:255], off
	global_load_dwordx4 v[236:239], v[196:197], off
	global_load_dwordx4 v[240:243], v[254:255], off offset:256
	global_load_dwordx4 v[244:247], v[196:197], off offset:256
	s_mov_b32 s6, 0x3c800000
	s_mov_b32 s2, 0xbfb8aa3b
	v_pk_mul_f32 v[16:17], v[160:161], s[6:7] op_sel_hi:[1,0]
	v_pk_mul_f32 v[22:23], v[158:159], s[6:7] op_sel_hi:[1,0]
	v_pk_mul_f32 v[24:25], v[156:157], s[6:7] op_sel_hi:[1,0]
	v_pk_mul_f32 v[26:27], v[154:155], s[6:7] op_sel_hi:[1,0]
	v_pk_mul_f32 v[22:23], v[22:23], s[2:3] op_sel_hi:[1,0]
	v_pk_mul_f32 v[16:17], v[16:17], s[2:3] op_sel_hi:[1,0]
	v_pk_mul_f32 v[26:27], v[26:27], s[2:3] op_sel_hi:[1,0]
	v_pk_mul_f32 v[24:25], v[24:25], s[2:3] op_sel_hi:[1,0]
	v_exp_f32_e32 v22, v22
	v_exp_f32_e32 v23, v23
	v_exp_f32_e32 v16, v16
	v_exp_f32_e32 v17, v17
	v_exp_f32_e32 v26, v26
	v_exp_f32_e32 v27, v27
	v_exp_f32_e32 v24, v24
	v_exp_f32_e32 v25, v25
	v_pk_add_f32 v[22:23], v[22:23], 1.0 op_sel_hi:[1,0]
	v_pk_add_f32 v[16:17], v[16:17], 1.0 op_sel_hi:[1,0]
	v_pk_add_f32 v[26:27], v[26:27], 1.0 op_sel_hi:[1,0]
	v_pk_add_f32 v[24:25], v[24:25], 1.0 op_sel_hi:[1,0]
	v_mbcnt_lo_u32_b32 v1, -1, 0
	v_rcp_f32_e32 v22, v22
	v_rcp_f32_e32 v23, v23
	v_rcp_f32_e32 v16, v16
	v_rcp_f32_e32 v17, v17
	v_rcp_f32_e32 v26, v26
	v_rcp_f32_e32 v27, v27
	v_rcp_f32_e32 v154, v24
	v_rcp_f32_e32 v155, v25
	v_mbcnt_hi_u32_b32 v166, -1, v1
	v_and_b32_e32 v28, 64, v166
	v_add_u32_e32 v167, 64, v28
	v_pk_mul_f32 v[146:147], v[146:147], s[6:7] op_sel_hi:[1,0]
	v_xor_b32_e32 v1, 16, v166
	v_pk_mul_f32 v[146:147], v[146:147], s[2:3] op_sel_hi:[1,0]
	v_cmp_lt_i32_e32 vcc, v1, v167
	v_exp_f32_e32 v146, v146
	v_exp_f32_e32 v147, v147
	v_cndmask_b32_e32 v1, v166, v1, vcc
	v_lshlrev_b32_e32 v1, 2, v1
	v_pk_add_f32 v[146:147], v[146:147], 1.0 op_sel_hi:[1,0]
	s_waitcnt vmcnt(12)
	v_lshlrev_b32_e32 v158, 16, v8
	v_lshlrev_b32_e32 v28, 16, v4
	v_and_b32_e32 v29, 0xffff0000, v4
	v_lshlrev_b32_e32 v4, 16, v5
	v_and_b32_e32 v5, 0xffff0000, v5
	v_lshlrev_b32_e32 v156, 16, v6
	v_and_b32_e32 v157, 0xffff0000, v6
	v_lshlrev_b32_e32 v6, 16, v7
	v_and_b32_e32 v7, 0xffff0000, v7
	v_and_b32_e32 v159, 0xffff0000, v8
	v_lshlrev_b32_e32 v8, 16, v9
	v_and_b32_e32 v9, 0xffff0000, v9
	v_lshlrev_b32_e32 v160, 16, v10
	v_and_b32_e32 v161, 0xffff0000, v10
	v_lshlrev_b32_e32 v10, 16, v11
	v_and_b32_e32 v11, 0xffff0000, v11
	v_pk_fma_f32 v[24:25], v[16:17], v[4:5], v[8:9]
	v_pk_fma_f32 v[28:29], v[22:23], v[28:29], v[158:159]
	v_pk_fma_f32 v[22:23], v[154:155], v[6:7], v[10:11]
	v_pk_fma_f32 v[26:27], v[26:27], v[156:157], v[160:161]
	v_mul_f32_e32 v4, v29, v29
	v_mul_f32_e32 v5, v25, v25
	v_mul_f32_e32 v6, v27, v27
	v_mul_f32_e32 v7, v23, v23
	v_fmac_f32_e32 v4, v28, v28
	v_fmac_f32_e32 v5, v24, v24
	v_fmac_f32_e32 v6, v26, v26
	v_fmac_f32_e32 v7, v22, v22
	v_add_f32_e32 v4, v4, v5
	v_add_f32_e32 v5, v6, v7
	v_lshlrev_b32_e32 v6, 16, v30
	v_and_b32_e32 v7, 0xffff0000, v30
	v_lshlrev_b32_e32 v8, 16, v31
	v_and_b32_e32 v9, 0xffff0000, v31
	v_pk_mul_f32 v[30:31], v[150:151], s[6:7] op_sel_hi:[1,0]
	v_pk_mul_f32 v[16:17], v[152:153], s[6:7] op_sel_hi:[1,0]
	v_pk_mul_f32 v[30:31], v[30:31], s[2:3] op_sel_hi:[1,0]
	v_lshlrev_b32_e32 v164, 16, v14
	v_exp_f32_e32 v30, v30
	v_exp_f32_e32 v31, v31
	v_and_b32_e32 v165, 0xffff0000, v14
	v_add_f32_e32 v154, v4, v5
	v_lshlrev_b32_e32 v4, 16, v15
	v_pk_add_f32 v[30:31], v[30:31], 1.0 op_sel_hi:[1,0]
	v_and_b32_e32 v5, 0xffff0000, v15
	v_lshlrev_b32_e32 v10, 16, v32
	v_and_b32_e32 v11, 0xffff0000, v32
	v_lshlrev_b32_e32 v14, 16, v33
	v_and_b32_e32 v15, 0xffff0000, v33
	v_pk_mul_f32 v[16:17], v[16:17], s[2:3] op_sel_hi:[1,0]
	v_rcp_f32_e32 v32, v30
	v_rcp_f32_e32 v33, v31
	v_pk_mul_f32 v[30:31], v[148:149], s[6:7] op_sel_hi:[1,0]
	v_exp_f32_e32 v16, v16
	v_exp_f32_e32 v17, v17
	v_pk_mul_f32 v[30:31], v[30:31], s[2:3] op_sel_hi:[1,0]
	v_rcp_f32_e32 v148, v146
	v_exp_f32_e32 v30, v30
	v_exp_f32_e32 v31, v31
	v_pk_add_f32 v[16:17], v[16:17], 1.0 op_sel_hi:[1,0]
	v_rcp_f32_e32 v149, v147
	v_rcp_f32_e32 v16, v16
	v_rcp_f32_e32 v17, v17
	v_pk_add_f32 v[30:31], v[30:31], 1.0 op_sel_hi:[1,0]
	v_lshlrev_b32_e32 v162, 16, v12
	v_rcp_f32_e32 v150, v30
	v_rcp_f32_e32 v151, v31
	v_and_b32_e32 v163, 0xffff0000, v12
	v_lshlrev_b32_e32 v12, 16, v13
	v_and_b32_e32 v13, 0xffff0000, v13
	v_pk_fma_f32 v[30:31], v[16:17], v[12:13], v[8:9]
	v_pk_fma_f32 v[32:33], v[32:33], v[162:163], v[6:7]
	v_pk_fma_f32 v[146:147], v[150:151], v[4:5], v[14:15]
	v_mul_f32_e32 v4, v33, v33
	v_mul_f32_e32 v5, v31, v31
	v_pk_fma_f32 v[148:149], v[148:149], v[164:165], v[10:11]
	v_fmac_f32_e32 v4, v32, v32
	v_fmac_f32_e32 v5, v30, v30
	v_add_f32_e32 v4, v4, v5
	v_mul_f32_e32 v5, v149, v149
	v_mul_f32_e32 v6, v147, v147
	v_fmac_f32_e32 v5, v148, v148
	v_fmac_f32_e32 v6, v146, v146
	v_add_f32_e32 v5, v5, v6
	v_add_f32_e32 v4, v4, v5
	v_add_f32_e32 v4, v154, v4
	v_mov_b32_e32 v6, v4
	s_nop 1
	v_permlane16_swap_b32 v6, v4
	s_nop 0
	v_xor_b32_e32 v5, 32, v166
	v_cmp_lt_i32_e32 vcc, v5, v167
	s_lshl_b32 s3, s5, 2
	s_add_i32 s5, s3, 0
	v_cndmask_b32_e32 v5, v166, v5, vcc
	v_lshlrev_b32_e32 v5, 2, v5
	s_waitcnt lgkmcnt(0)
	v_add_f32_e32 v6, v4, v6
	v_mov_b32_e32 v7, v6
	s_nop 1
	v_permlane32_swap_b32 v7, v6
	s_nop 0
	v_cmp_gt_u32_e32 vcc, 16, v198
	v_lshl_add_u32 v4, v189, 4, s5
	s_and_saveexec_b64 s[20:21], vcc
	s_cbranch_execz .LBB0_1535
	s_waitcnt lgkmcnt(0)
	v_add_f32_e32 v6, v6, v7
	ds_write_b32 v4, v6
.LBB0_1535:
	s_or_b64 exec, exec, s[20:21]
	s_waitcnt lgkmcnt(0)
	s_waitcnt vmcnt(8)
	v_mov_b64_e32 v[6:7], v[200:201]
	v_mov_b64_e32 v[8:9], v[202:203]
	v_mov_b64_e32 v[10:11], v[204:205]
	v_mov_b64_e32 v[12:13], v[206:207]
	v_mov_b64_e32 v[14:15], v[208:209]
	v_mov_b64_e32 v[16:17], v[210:211]
	v_mov_b64_e32 v[150:151], v[212:213]
	v_mov_b64_e32 v[152:153], v[214:215]
	v_lshl_add_u64 v[254:255], v[254:255], 0, v[250:251]
	v_lshl_add_u64 v[196:197], v[196:197], 0, v[250:251]
	v_lshl_add_u64 v[254:255], v[254:255], 0, v[250:251]
	v_lshl_add_u64 v[196:197], v[196:197], 0, v[250:251]
	v_lshl_add_u64 v[254:255], v[254:255], 0, v[250:251]
	v_lshl_add_u64 v[196:197], v[196:197], 0, v[250:251]
	v_lshl_add_u64 v[254:255], v[254:255], 0, v[250:251]
	v_lshl_add_u64 v[196:197], v[196:197], 0, v[250:251]
	v_lshl_add_u64 v[254:255], v[254:255], 0, v[250:251]
	v_lshl_add_u64 v[196:197], v[196:197], 0, v[250:251]
	global_load_dwordx4 v[200:203], v[254:255], off
	global_load_dwordx4 v[204:207], v[196:197], off
	global_load_dwordx4 v[208:211], v[254:255], off offset:256
	global_load_dwordx4 v[212:215], v[196:197], off offset:256
	v_pk_mul_f32 v[144:145], v[144:145], s[6:7] op_sel_hi:[1,0]
	v_pk_mul_f32 v[142:143], v[142:143], s[6:7] op_sel_hi:[1,0]
	v_pk_mul_f32 v[140:141], v[140:141], s[6:7] op_sel_hi:[1,0]
	v_pk_mul_f32 v[138:139], v[138:139], s[6:7] op_sel_hi:[1,0]
	v_pk_mul_f32 v[136:137], v[136:137], s[6:7] op_sel_hi:[1,0]
	v_pk_mul_f32 v[142:143], v[142:143], s[2:3] op_sel_hi:[1,0]
	v_pk_mul_f32 v[144:145], v[144:145], s[2:3] op_sel_hi:[1,0]
	v_pk_mul_f32 v[138:139], v[138:139], s[2:3] op_sel_hi:[1,0]
	v_pk_mul_f32 v[140:141], v[140:141], s[2:3] op_sel_hi:[1,0]
	v_pk_mul_f32 v[154:155], v[136:137], s[2:3] op_sel_hi:[1,0]
	v_exp_f32_e32 v136, v142
	v_exp_f32_e32 v137, v143
	v_exp_f32_e32 v142, v144
	v_exp_f32_e32 v143, v145
	v_exp_f32_e32 v138, v138
	v_exp_f32_e32 v139, v139
	v_exp_f32_e32 v140, v140
	v_exp_f32_e32 v141, v141
	v_pk_mul_f32 v[134:135], v[134:135], s[6:7] op_sel_hi:[1,0]
	v_pk_add_f32 v[138:139], v[138:139], 1.0 op_sel_hi:[1,0]
	v_pk_mul_f32 v[134:135], v[134:135], s[2:3] op_sel_hi:[1,0]
	v_pk_add_f32 v[140:141], v[140:141], 1.0 op_sel_hi:[1,0]
	v_exp_f32_e32 v144, v134
	v_exp_f32_e32 v145, v135
	v_pk_add_f32 v[134:135], v[136:137], 1.0 op_sel_hi:[1,0]
	v_pk_add_f32 v[136:137], v[142:143], 1.0 op_sel_hi:[1,0]
	v_rcp_f32_e32 v134, v134
	v_rcp_f32_e32 v135, v135
	v_rcp_f32_e32 v136, v136
	v_rcp_f32_e32 v137, v137
	v_rcp_f32_e32 v138, v138
	v_rcp_f32_e32 v139, v139
	v_rcp_f32_e32 v142, v140
	v_rcp_f32_e32 v143, v141
	v_lshlrev_b32_e32 v158, 16, v10
	v_lshlrev_b32_e32 v140, 16, v6
	v_and_b32_e32 v141, 0xffff0000, v6
	v_lshlrev_b32_e32 v6, 16, v7
	v_and_b32_e32 v7, 0xffff0000, v7
	v_lshlrev_b32_e32 v156, 16, v8
	v_and_b32_e32 v157, 0xffff0000, v8
	v_lshlrev_b32_e32 v8, 16, v9
	v_and_b32_e32 v9, 0xffff0000, v9
	v_and_b32_e32 v159, 0xffff0000, v10
	v_lshlrev_b32_e32 v10, 16, v11
	v_and_b32_e32 v11, 0xffff0000, v11
	v_lshlrev_b32_e32 v160, 16, v12
	v_and_b32_e32 v161, 0xffff0000, v12
	v_lshlrev_b32_e32 v12, 16, v13
	v_and_b32_e32 v13, 0xffff0000, v13
	v_pk_fma_f32 v[136:137], v[136:137], v[6:7], v[10:11]
	v_pk_fma_f32 v[140:141], v[134:135], v[140:141], v[158:159]
	v_pk_fma_f32 v[134:135], v[142:143], v[8:9], v[12:13]
	v_pk_fma_f32 v[138:139], v[138:139], v[156:157], v[160:161]
	v_mul_f32_e32 v6, v141, v141
	v_mul_f32_e32 v7, v137, v137
	v_mul_f32_e32 v8, v139, v139
	v_mul_f32_e32 v9, v135, v135
	v_fmac_f32_e32 v6, v140, v140
	v_fmac_f32_e32 v7, v136, v136
	v_fmac_f32_e32 v8, v138, v138
	v_fmac_f32_e32 v9, v134, v134
	v_add_f32_e32 v6, v6, v7
	v_add_f32_e32 v7, v8, v9
	v_add_f32_e32 v156, v6, v7
	v_exp_f32_e32 v6, v154
	v_exp_f32_e32 v7, v155
	v_pk_mul_f32 v[10:11], v[132:133], s[6:7] op_sel_hi:[1,0]
	v_pk_mul_f32 v[12:13], v[130:131], s[6:7] op_sel_hi:[1,0]
	v_pk_mul_f32 v[10:11], v[10:11], s[2:3] op_sel_hi:[1,0]
	v_pk_mul_f32 v[12:13], v[12:13], s[2:3] op_sel_hi:[1,0]
	v_exp_f32_e32 v10, v10
	v_exp_f32_e32 v12, v12
	v_exp_f32_e32 v13, v13
	v_exp_f32_e32 v11, v11
	v_pk_add_f32 v[8:9], v[144:145], 1.0 op_sel_hi:[1,0]
	v_pk_add_f32 v[6:7], v[6:7], 1.0 op_sel_hi:[1,0]
	v_rcp_f32_e32 v8, v8
	v_rcp_f32_e32 v9, v9
	v_rcp_f32_e32 v6, v6
	v_rcp_f32_e32 v7, v7
	v_pk_add_f32 v[12:13], v[12:13], 1.0 op_sel_hi:[1,0]
	v_pk_add_f32 v[10:11], v[10:11], 1.0 op_sel_hi:[1,0]
	v_rcp_f32_e32 v12, v12
	v_rcp_f32_e32 v10, v10
	v_rcp_f32_e32 v11, v11
	v_rcp_f32_e32 v13, v13
	v_lshlrev_b32_e32 v162, 16, v14
	v_and_b32_e32 v163, 0xffff0000, v14
	v_lshlrev_b32_e32 v14, 16, v15
	v_and_b32_e32 v15, 0xffff0000, v15
	v_lshlrev_b32_e32 v166, 16, v150
	v_and_b32_e32 v167, 0xffff0000, v150
	v_lshlrev_b32_e32 v150, 16, v151
	v_and_b32_e32 v151, 0xffff0000, v151
	v_pk_fma_f32 v[130:131], v[6:7], v[14:15], v[150:151]
	v_pk_fma_f32 v[132:133], v[8:9], v[162:163], v[166:167]
	v_lshlrev_b32_e32 v164, 16, v16
	v_and_b32_e32 v165, 0xffff0000, v16
	v_lshlrev_b32_e32 v16, 16, v17
	v_and_b32_e32 v17, 0xffff0000, v17
	v_lshlrev_b32_e32 v168, 16, v152
	v_and_b32_e32 v169, 0xffff0000, v152
	v_lshlrev_b32_e32 v152, 16, v153
	v_and_b32_e32 v153, 0xffff0000, v153
	v_mul_f32_e32 v6, v133, v133
	v_mul_f32_e32 v7, v131, v131
	v_pk_fma_f32 v[142:143], v[10:11], v[16:17], v[152:153]
	v_pk_fma_f32 v[144:145], v[12:13], v[164:165], v[168:169]
	v_fmac_f32_e32 v6, v132, v132
	v_fmac_f32_e32 v7, v130, v130
	v_add_f32_e32 v6, v6, v7
	v_mul_f32_e32 v7, v145, v145
	v_mul_f32_e32 v8, v143, v143
	v_fmac_f32_e32 v7, v144, v144
	v_fmac_f32_e32 v8, v142, v142
	v_add_f32_e32 v7, v7, v8
	v_add_f32_e32 v6, v6, v7
	v_add_f32_e32 v6, v156, v6
	v_mov_b32_e32 v7, v6
	s_nop 1
	v_permlane16_swap_b32 v7, v6
	s_nop 0
	s_waitcnt lgkmcnt(0)
	v_add_f32_e32 v6, v6, v7
	v_mov_b32_e32 v7, v6
	s_nop 1
	v_permlane32_swap_b32 v7, v6
	s_nop 0
	s_and_saveexec_b64 s[2:3], vcc
	s_cbranch_execz .LBB0_1537
	s_waitcnt lgkmcnt(0)
	v_add_f32_e32 v6, v6, v7
	ds_write_b32 v4, v6 offset:256
.LBB0_1537:
	s_or_b64 exec, exec, s[2:3]
	s_waitcnt lgkmcnt(0)
	s_waitcnt vmcnt(8)
	v_mov_b64_e32 v[6:7], v[216:217]
	v_mov_b64_e32 v[8:9], v[218:219]
	v_mov_b64_e32 v[10:11], v[220:221]
	v_mov_b64_e32 v[12:13], v[222:223]
	v_mov_b64_e32 v[14:15], v[224:225]
	v_mov_b64_e32 v[16:17], v[226:227]
	v_mov_b64_e32 v[150:151], v[228:229]
	v_mov_b64_e32 v[152:153], v[230:231]
	v_lshl_add_u64 v[254:255], v[254:255], 0, v[250:251]
	v_lshl_add_u64 v[196:197], v[196:197], 0, v[250:251]
	global_load_dwordx4 v[216:219], v[254:255], off
	global_load_dwordx4 v[220:223], v[196:197], off
	global_load_dwordx4 v[224:227], v[254:255], off offset:256
	global_load_dwordx4 v[228:231], v[196:197], off offset:256
	s_mov_b32 s2, 0xbfb8aa3b
	v_pk_mul_f32 v[128:129], v[128:129], s[6:7] op_sel_hi:[1,0]
	v_pk_mul_f32 v[126:127], v[126:127], s[6:7] op_sel_hi:[1,0]
	v_pk_mul_f32 v[124:125], v[124:125], s[6:7] op_sel_hi:[1,0]
	v_pk_mul_f32 v[122:123], v[122:123], s[6:7] op_sel_hi:[1,0]
	v_pk_mul_f32 v[154:155], v[120:121], s[6:7] op_sel_hi:[1,0]
	v_pk_mul_f32 v[118:119], v[118:119], s[6:7] op_sel_hi:[1,0]
	v_pk_mul_f32 v[120:121], v[126:127], s[2:3] op_sel_hi:[1,0]
	v_pk_mul_f32 v[126:127], v[128:129], s[2:3] op_sel_hi:[1,0]
	v_pk_mul_f32 v[122:123], v[122:123], s[2:3] op_sel_hi:[1,0]
	v_pk_mul_f32 v[124:125], v[124:125], s[2:3] op_sel_hi:[1,0]
	v_pk_mul_f32 v[128:129], v[118:119], s[2:3] op_sel_hi:[1,0]
	v_exp_f32_e32 v118, v120
	v_exp_f32_e32 v119, v121
	v_exp_f32_e32 v120, v126
	v_exp_f32_e32 v121, v127
	v_exp_f32_e32 v122, v122
	v_exp_f32_e32 v123, v123
	v_exp_f32_e32 v124, v124
	v_exp_f32_e32 v125, v125
	v_pk_add_f32 v[118:119], v[118:119], 1.0 op_sel_hi:[1,0]
	v_pk_add_f32 v[120:121], v[120:121], 1.0 op_sel_hi:[1,0]
	v_pk_add_f32 v[122:123], v[122:123], 1.0 op_sel_hi:[1,0]
	v_pk_add_f32 v[124:125], v[124:125], 1.0 op_sel_hi:[1,0]
	v_rcp_f32_e32 v118, v118
	v_rcp_f32_e32 v119, v119
	v_rcp_f32_e32 v120, v120
	v_rcp_f32_e32 v121, v121
	v_rcp_f32_e32 v122, v122
	v_rcp_f32_e32 v123, v123
	v_rcp_f32_e32 v156, v124
	v_rcp_f32_e32 v157, v125
	v_exp_f32_e32 v126, v128
	v_exp_f32_e32 v127, v129
	v_lshlrev_b32_e32 v160, 16, v10
	v_lshlrev_b32_e32 v124, 16, v6
	v_and_b32_e32 v125, 0xffff0000, v6
	v_lshlrev_b32_e32 v6, 16, v7
	v_and_b32_e32 v7, 0xffff0000, v7
	v_lshlrev_b32_e32 v158, 16, v8
	v_and_b32_e32 v159, 0xffff0000, v8
	v_lshlrev_b32_e32 v8, 16, v9
	v_and_b32_e32 v9, 0xffff0000, v9
	v_and_b32_e32 v161, 0xffff0000, v10
	v_lshlrev_b32_e32 v10, 16, v11
	v_and_b32_e32 v11, 0xffff0000, v11
	v_lshlrev_b32_e32 v162, 16, v12
	v_and_b32_e32 v163, 0xffff0000, v12
	v_lshlrev_b32_e32 v12, 16, v13
	v_and_b32_e32 v13, 0xffff0000, v13
	v_pk_fma_f32 v[120:121], v[120:121], v[6:7], v[10:11]
	v_pk_fma_f32 v[124:125], v[118:119], v[124:125], v[160:161]
	v_pk_fma_f32 v[118:119], v[156:157], v[8:9], v[12:13]
	v_pk_fma_f32 v[122:123], v[122:123], v[158:159], v[162:163]
	v_mul_f32_e32 v6, v125, v125
	v_mul_f32_e32 v7, v121, v121
	v_mul_f32_e32 v8, v123, v123
	v_mul_f32_e32 v9, v119, v119
	v_fmac_f32_e32 v6, v124, v124
	v_fmac_f32_e32 v7, v120, v120
	v_fmac_f32_e32 v8, v122, v122
	v_fmac_f32_e32 v9, v118, v118
	v_add_f32_e32 v6, v6, v7
	v_add_f32_e32 v7, v8, v9
	v_add_f32_e32 v156, v6, v7
	v_pk_mul_f32 v[6:7], v[154:155], s[2:3] op_sel_hi:[1,0]
	v_pk_mul_f32 v[10:11], v[116:117], s[6:7] op_sel_hi:[1,0]
	v_exp_f32_e32 v6, v6
	v_exp_f32_e32 v7, v7
	v_pk_mul_f32 v[12:13], v[114:115], s[6:7] op_sel_hi:[1,0]
	v_pk_mul_f32 v[10:11], v[10:11], s[2:3] op_sel_hi:[1,0]
	v_pk_mul_f32 v[12:13], v[12:13], s[2:3] op_sel_hi:[1,0]
	v_exp_f32_e32 v10, v10
	v_exp_f32_e32 v12, v12
	v_exp_f32_e32 v13, v13
	v_exp_f32_e32 v11, v11
	v_pk_add_f32 v[8:9], v[126:127], 1.0 op_sel_hi:[1,0]
	v_pk_add_f32 v[6:7], v[6:7], 1.0 op_sel_hi:[1,0]
	v_rcp_f32_e32 v8, v8
	v_rcp_f32_e32 v9, v9
	v_rcp_f32_e32 v6, v6
	v_rcp_f32_e32 v7, v7
	v_pk_add_f32 v[12:13], v[12:13], 1.0 op_sel_hi:[1,0]
	v_pk_add_f32 v[10:11], v[10:11], 1.0 op_sel_hi:[1,0]
	v_rcp_f32_e32 v12, v12
	v_rcp_f32_e32 v10, v10
	v_rcp_f32_e32 v11, v11
	v_rcp_f32_e32 v13, v13
	v_lshlrev_b32_e32 v164, 16, v14
	v_and_b32_e32 v165, 0xffff0000, v14
	v_lshlrev_b32_e32 v14, 16, v15
	v_and_b32_e32 v15, 0xffff0000, v15
	v_lshlrev_b32_e32 v168, 16, v150
	v_and_b32_e32 v169, 0xffff0000, v150
	v_lshlrev_b32_e32 v150, 16, v151
	v_and_b32_e32 v151, 0xffff0000, v151
	v_pk_fma_f32 v[114:115], v[6:7], v[14:15], v[150:151]
	v_pk_fma_f32 v[116:117], v[8:9], v[164:165], v[168:169]
	v_lshlrev_b32_e32 v166, 16, v16
	v_and_b32_e32 v167, 0xffff0000, v16
	v_lshlrev_b32_e32 v16, 16, v17
	v_and_b32_e32 v17, 0xffff0000, v17
	v_lshlrev_b32_e32 v170, 16, v152
	v_and_b32_e32 v171, 0xffff0000, v152
	v_lshlrev_b32_e32 v152, 16, v153
	v_and_b32_e32 v153, 0xffff0000, v153
	v_mul_f32_e32 v6, v117, v117
	v_mul_f32_e32 v7, v115, v115
	v_pk_fma_f32 v[126:127], v[10:11], v[16:17], v[152:153]
	v_pk_fma_f32 v[128:129], v[12:13], v[166:167], v[170:171]
	v_fmac_f32_e32 v6, v116, v116
	v_fmac_f32_e32 v7, v114, v114
	v_add_f32_e32 v6, v6, v7
	v_mul_f32_e32 v7, v129, v129
	v_mul_f32_e32 v8, v127, v127
	v_fmac_f32_e32 v7, v128, v128
	v_fmac_f32_e32 v8, v126, v126
	v_add_f32_e32 v7, v7, v8
	v_add_f32_e32 v6, v6, v7
	v_add_f32_e32 v6, v156, v6
	v_mov_b32_e32 v7, v6
	s_nop 1
	v_permlane16_swap_b32 v7, v6
	s_nop 0
	s_waitcnt lgkmcnt(0)
	v_add_f32_e32 v6, v6, v7
	v_mov_b32_e32 v7, v6
	s_nop 1
	v_permlane32_swap_b32 v7, v6
	s_nop 0
	s_and_saveexec_b64 s[20:21], vcc
	s_cbranch_execz .LBB0_1539
	s_waitcnt lgkmcnt(0)
	v_add_f32_e32 v6, v6, v7
	ds_write_b32 v4, v6 offset:512
.LBB0_1539:
	s_or_b64 exec, exec, s[20:21]
	s_waitcnt lgkmcnt(0)
	s_waitcnt vmcnt(8)
	v_mov_b64_e32 v[6:7], v[232:233]
	v_mov_b64_e32 v[8:9], v[234:235]
	v_mov_b64_e32 v[10:11], v[236:237]
	v_mov_b64_e32 v[12:13], v[238:239]
	v_mov_b64_e32 v[14:15], v[240:241]
	v_mov_b64_e32 v[16:17], v[242:243]
	v_mov_b64_e32 v[150:151], v[244:245]
	v_mov_b64_e32 v[152:153], v[246:247]
	v_lshl_add_u64 v[254:255], v[254:255], 0, v[250:251]
	v_lshl_add_u64 v[196:197], v[196:197], 0, v[250:251]
	global_load_dwordx4 v[232:235], v[254:255], off
	global_load_dwordx4 v[236:239], v[196:197], off
	global_load_dwordx4 v[240:243], v[254:255], off offset:256
	global_load_dwordx4 v[244:247], v[196:197], off offset:256
	v_pk_mul_f32 v[112:113], v[112:113], s[6:7] op_sel_hi:[1,0]
	v_pk_mul_f32 v[110:111], v[110:111], s[6:7] op_sel_hi:[1,0]
	v_pk_mul_f32 v[108:109], v[108:109], s[6:7] op_sel_hi:[1,0]
	v_pk_mul_f32 v[106:107], v[106:107], s[6:7] op_sel_hi:[1,0]
	v_pk_mul_f32 v[104:105], v[104:105], s[6:7] op_sel_hi:[1,0]
	v_pk_mul_f32 v[110:111], v[110:111], s[2:3] op_sel_hi:[1,0]
	v_pk_mul_f32 v[112:113], v[112:113], s[2:3] op_sel_hi:[1,0]
	v_pk_mul_f32 v[106:107], v[106:107], s[2:3] op_sel_hi:[1,0]
	v_pk_mul_f32 v[108:109], v[108:109], s[2:3] op_sel_hi:[1,0]
	v_pk_mul_f32 v[154:155], v[104:105], s[2:3] op_sel_hi:[1,0]
	v_exp_f32_e32 v104, v110
	v_exp_f32_e32 v105, v111
	v_exp_f32_e32 v110, v112
	v_exp_f32_e32 v111, v113
	v_exp_f32_e32 v106, v106
	v_exp_f32_e32 v107, v107
	v_exp_f32_e32 v108, v108
	v_exp_f32_e32 v109, v109
	v_pk_mul_f32 v[102:103], v[102:103], s[6:7] op_sel_hi:[1,0]
	v_pk_add_f32 v[106:107], v[106:107], 1.0 op_sel_hi:[1,0]
	v_pk_mul_f32 v[102:103], v[102:103], s[2:3] op_sel_hi:[1,0]
	v_pk_add_f32 v[108:109], v[108:109], 1.0 op_sel_hi:[1,0]
	v_exp_f32_e32 v112, v102
	v_exp_f32_e32 v113, v103
	v_pk_add_f32 v[102:103], v[104:105], 1.0 op_sel_hi:[1,0]
	v_pk_add_f32 v[104:105], v[110:111], 1.0 op_sel_hi:[1,0]
	v_rcp_f32_e32 v102, v102
	v_rcp_f32_e32 v103, v103
	v_rcp_f32_e32 v104, v104
	v_rcp_f32_e32 v105, v105
	v_rcp_f32_e32 v110, v106
	v_rcp_f32_e32 v111, v107
	v_rcp_f32_e32 v156, v108
	v_rcp_f32_e32 v157, v109
	v_lshlrev_b32_e32 v160, 16, v10
	v_lshlrev_b32_e32 v108, 16, v6
	v_and_b32_e32 v109, 0xffff0000, v6
	v_lshlrev_b32_e32 v6, 16, v7
	v_and_b32_e32 v7, 0xffff0000, v7
	v_lshlrev_b32_e32 v158, 16, v8
	v_and_b32_e32 v159, 0xffff0000, v8
	v_lshlrev_b32_e32 v8, 16, v9
	v_and_b32_e32 v9, 0xffff0000, v9
	v_and_b32_e32 v161, 0xffff0000, v10
	v_lshlrev_b32_e32 v10, 16, v11
	v_and_b32_e32 v11, 0xffff0000, v11
	v_lshlrev_b32_e32 v162, 16, v12
	v_and_b32_e32 v163, 0xffff0000, v12
	v_lshlrev_b32_e32 v12, 16, v13
	v_and_b32_e32 v13, 0xffff0000, v13
	v_pk_fma_f32 v[106:107], v[104:105], v[6:7], v[10:11]
	v_pk_fma_f32 v[108:109], v[102:103], v[108:109], v[160:161]
	v_pk_fma_f32 v[102:103], v[156:157], v[8:9], v[12:13]
	v_pk_fma_f32 v[104:105], v[110:111], v[158:159], v[162:163]
	v_mul_f32_e32 v6, v109, v109
	v_mul_f32_e32 v7, v107, v107
	v_mul_f32_e32 v8, v105, v105
	v_mul_f32_e32 v9, v103, v103
	v_fmac_f32_e32 v6, v108, v108
	v_fmac_f32_e32 v7, v106, v106
	v_fmac_f32_e32 v8, v104, v104
	v_fmac_f32_e32 v9, v102, v102
	v_add_f32_e32 v6, v6, v7
	v_add_f32_e32 v7, v8, v9
	v_add_f32_e32 v156, v6, v7
	v_exp_f32_e32 v6, v154
	v_exp_f32_e32 v7, v155
	v_pk_mul_f32 v[10:11], v[100:101], s[6:7] op_sel_hi:[1,0]
	v_pk_mul_f32 v[12:13], v[98:99], s[6:7] op_sel_hi:[1,0]
	v_pk_mul_f32 v[10:11], v[10:11], s[2:3] op_sel_hi:[1,0]
	v_pk_mul_f32 v[12:13], v[12:13], s[2:3] op_sel_hi:[1,0]
	v_exp_f32_e32 v10, v10
	v_exp_f32_e32 v12, v12
	v_exp_f32_e32 v13, v13
	v_exp_f32_e32 v11, v11
	v_pk_add_f32 v[8:9], v[112:113], 1.0 op_sel_hi:[1,0]
	v_pk_add_f32 v[6:7], v[6:7], 1.0 op_sel_hi:[1,0]
	v_rcp_f32_e32 v8, v8
	v_rcp_f32_e32 v9, v9
	v_rcp_f32_e32 v6, v6
	v_rcp_f32_e32 v7, v7
	v_pk_add_f32 v[12:13], v[12:13], 1.0 op_sel_hi:[1,0]
	v_pk_add_f32 v[10:11], v[10:11], 1.0 op_sel_hi:[1,0]
	v_rcp_f32_e32 v12, v12
	v_rcp_f32_e32 v10, v10
	v_rcp_f32_e32 v11, v11
	v_rcp_f32_e32 v13, v13
	v_lshlrev_b32_e32 v164, 16, v14
	v_and_b32_e32 v165, 0xffff0000, v14
	v_lshlrev_b32_e32 v14, 16, v15
	v_and_b32_e32 v15, 0xffff0000, v15
	v_lshlrev_b32_e32 v168, 16, v150
	v_and_b32_e32 v169, 0xffff0000, v150
	v_lshlrev_b32_e32 v150, 16, v151
	v_and_b32_e32 v151, 0xffff0000, v151
	v_pk_fma_f32 v[100:101], v[6:7], v[14:15], v[150:151]
	v_pk_fma_f32 v[110:111], v[8:9], v[164:165], v[168:169]
	v_lshlrev_b32_e32 v166, 16, v16
	v_and_b32_e32 v167, 0xffff0000, v16
	v_lshlrev_b32_e32 v16, 16, v17
	v_and_b32_e32 v17, 0xffff0000, v17
	v_lshlrev_b32_e32 v170, 16, v152
	v_and_b32_e32 v171, 0xffff0000, v152
	v_lshlrev_b32_e32 v152, 16, v153
	v_and_b32_e32 v153, 0xffff0000, v153
	v_mul_f32_e32 v6, v111, v111
	v_mul_f32_e32 v7, v101, v101
	v_pk_fma_f32 v[98:99], v[10:11], v[16:17], v[152:153]
	v_pk_fma_f32 v[112:113], v[12:13], v[166:167], v[170:171]
	v_fmac_f32_e32 v6, v110, v110
	v_fmac_f32_e32 v7, v100, v100
	v_add_f32_e32 v6, v6, v7
	v_mul_f32_e32 v7, v113, v113
	v_mul_f32_e32 v8, v99, v99
	v_fmac_f32_e32 v7, v112, v112
	v_fmac_f32_e32 v8, v98, v98
	v_add_f32_e32 v7, v7, v8
	v_add_f32_e32 v6, v6, v7
	v_add_f32_e32 v6, v156, v6
	v_mov_b32_e32 v7, v6
	s_nop 1
	v_permlane16_swap_b32 v7, v6
	s_nop 0
	s_waitcnt lgkmcnt(0)
	v_add_f32_e32 v6, v6, v7
	v_mov_b32_e32 v7, v6
	s_nop 1
	v_permlane32_swap_b32 v7, v6
	s_nop 0
	s_and_saveexec_b64 s[2:3], vcc
	s_cbranch_execz .LBB0_1541
	s_waitcnt lgkmcnt(0)
	v_add_f32_e32 v6, v6, v7
	ds_write_b32 v4, v6 offset:768
.LBB0_1541:
	s_or_b64 exec, exec, s[2:3]
	s_waitcnt lgkmcnt(0)
	s_waitcnt vmcnt(8)
	v_mov_b64_e32 v[6:7], v[200:201]
	v_mov_b64_e32 v[8:9], v[202:203]
	v_mov_b64_e32 v[10:11], v[204:205]
	v_mov_b64_e32 v[12:13], v[206:207]
	v_mov_b64_e32 v[14:15], v[208:209]
	v_mov_b64_e32 v[16:17], v[210:211]
	v_mov_b64_e32 v[150:151], v[212:213]
	v_mov_b64_e32 v[152:153], v[214:215]
	v_lshl_add_u64 v[254:255], v[254:255], 0, v[250:251]
	v_lshl_add_u64 v[196:197], v[196:197], 0, v[250:251]
	global_load_dwordx4 v[200:203], v[254:255], off
	global_load_dwordx4 v[204:207], v[196:197], off
	global_load_dwordx4 v[208:211], v[254:255], off offset:256
	global_load_dwordx4 v[212:215], v[196:197], off offset:256
	s_mov_b32 s2, 0xbfb8aa3b
	v_pk_mul_f32 v[96:97], v[96:97], s[6:7] op_sel_hi:[1,0]
	v_pk_mul_f32 v[94:95], v[94:95], s[6:7] op_sel_hi:[1,0]
	v_pk_mul_f32 v[92:93], v[92:93], s[6:7] op_sel_hi:[1,0]
	v_pk_mul_f32 v[90:91], v[90:91], s[6:7] op_sel_hi:[1,0]
	v_pk_mul_f32 v[154:155], v[88:89], s[6:7] op_sel_hi:[1,0]
	v_pk_mul_f32 v[86:87], v[86:87], s[6:7] op_sel_hi:[1,0]
	v_pk_mul_f32 v[88:89], v[94:95], s[2:3] op_sel_hi:[1,0]
	v_pk_mul_f32 v[94:95], v[96:97], s[2:3] op_sel_hi:[1,0]
	v_pk_mul_f32 v[90:91], v[90:91], s[2:3] op_sel_hi:[1,0]
	v_pk_mul_f32 v[92:93], v[92:93], s[2:3] op_sel_hi:[1,0]
	v_pk_mul_f32 v[96:97], v[86:87], s[2:3] op_sel_hi:[1,0]
	v_exp_f32_e32 v86, v88
	v_exp_f32_e32 v87, v89
	v_exp_f32_e32 v88, v94
	v_exp_f32_e32 v89, v95
	v_exp_f32_e32 v90, v90
	v_exp_f32_e32 v91, v91
	v_exp_f32_e32 v92, v92
	v_exp_f32_e32 v93, v93
	v_pk_add_f32 v[86:87], v[86:87], 1.0 op_sel_hi:[1,0]
	v_pk_add_f32 v[88:89], v[88:89], 1.0 op_sel_hi:[1,0]
	v_pk_add_f32 v[90:91], v[90:91], 1.0 op_sel_hi:[1,0]
	v_pk_add_f32 v[92:93], v[92:93], 1.0 op_sel_hi:[1,0]
	v_rcp_f32_e32 v86, v86
	v_rcp_f32_e32 v87, v87
	v_rcp_f32_e32 v88, v88
	v_rcp_f32_e32 v89, v89
	v_rcp_f32_e32 v94, v90
	v_rcp_f32_e32 v95, v91
	v_rcp_f32_e32 v156, v92
	v_rcp_f32_e32 v157, v93
	v_lshlrev_b32_e32 v160, 16, v10
	v_lshlrev_b32_e32 v92, 16, v6
	v_and_b32_e32 v93, 0xffff0000, v6
	v_lshlrev_b32_e32 v6, 16, v7
	v_and_b32_e32 v7, 0xffff0000, v7
	v_lshlrev_b32_e32 v158, 16, v8
	v_and_b32_e32 v159, 0xffff0000, v8
	v_lshlrev_b32_e32 v8, 16, v9
	v_and_b32_e32 v9, 0xffff0000, v9
	v_and_b32_e32 v161, 0xffff0000, v10
	v_lshlrev_b32_e32 v10, 16, v11
	v_and_b32_e32 v11, 0xffff0000, v11
	v_lshlrev_b32_e32 v162, 16, v12
	v_and_b32_e32 v163, 0xffff0000, v12
	v_lshlrev_b32_e32 v12, 16, v13
	v_and_b32_e32 v13, 0xffff0000, v13
	v_pk_fma_f32 v[90:91], v[88:89], v[6:7], v[10:11]
	v_pk_fma_f32 v[92:93], v[86:87], v[92:93], v[160:161]
	v_pk_fma_f32 v[86:87], v[156:157], v[8:9], v[12:13]
	v_pk_fma_f32 v[88:89], v[94:95], v[158:159], v[162:163]
	v_mul_f32_e32 v6, v93, v93
	v_mul_f32_e32 v7, v91, v91
	v_mul_f32_e32 v8, v89, v89
	v_mul_f32_e32 v9, v87, v87
	v_fmac_f32_e32 v6, v92, v92
	v_fmac_f32_e32 v7, v90, v90
	v_fmac_f32_e32 v8, v88, v88
	v_fmac_f32_e32 v9, v86, v86
	v_add_f32_e32 v6, v6, v7
	v_add_f32_e32 v7, v8, v9
	v_pk_mul_f32 v[8:9], v[154:155], s[2:3] op_sel_hi:[1,0]
	v_add_f32_e32 v19, v6, v7
	v_exp_f32_e32 v6, v96
	v_exp_f32_e32 v7, v97
	v_exp_f32_e32 v8, v8
	v_exp_f32_e32 v9, v9
	v_pk_mul_f32 v[10:11], v[84:85], s[6:7] op_sel_hi:[1,0]
	v_pk_mul_f32 v[12:13], v[82:83], s[6:7] op_sel_hi:[1,0]
	v_pk_mul_f32 v[10:11], v[10:11], s[2:3] op_sel_hi:[1,0]
	v_pk_mul_f32 v[12:13], v[12:13], s[2:3] op_sel_hi:[1,0]
	v_exp_f32_e32 v10, v10
	v_exp_f32_e32 v12, v12
	v_exp_f32_e32 v13, v13
	v_exp_f32_e32 v11, v11
	v_pk_add_f32 v[6:7], v[6:7], 1.0 op_sel_hi:[1,0]
	v_pk_add_f32 v[8:9], v[8:9], 1.0 op_sel_hi:[1,0]
	v_rcp_f32_e32 v6, v6
	v_rcp_f32_e32 v7, v7
	v_rcp_f32_e32 v8, v8
	v_rcp_f32_e32 v9, v9
	v_pk_add_f32 v[12:13], v[12:13], 1.0 op_sel_hi:[1,0]
	v_pk_add_f32 v[10:11], v[10:11], 1.0 op_sel_hi:[1,0]
	v_rcp_f32_e32 v12, v12
	v_rcp_f32_e32 v10, v10
	v_rcp_f32_e32 v11, v11
	v_rcp_f32_e32 v13, v13
	v_lshlrev_b32_e32 v164, 16, v14
	v_and_b32_e32 v165, 0xffff0000, v14
	v_lshlrev_b32_e32 v14, 16, v15
	v_and_b32_e32 v15, 0xffff0000, v15
	v_lshlrev_b32_e32 v168, 16, v150
	v_and_b32_e32 v169, 0xffff0000, v150
	v_lshlrev_b32_e32 v150, 16, v151
	v_and_b32_e32 v151, 0xffff0000, v151
	v_pk_fma_f32 v[84:85], v[8:9], v[14:15], v[150:151]
	v_pk_fma_f32 v[94:95], v[6:7], v[164:165], v[168:169]
	v_lshlrev_b32_e32 v166, 16, v16
	v_and_b32_e32 v167, 0xffff0000, v16
	v_lshlrev_b32_e32 v16, 16, v17
	v_and_b32_e32 v17, 0xffff0000, v17
	v_lshlrev_b32_e32 v170, 16, v152
	v_and_b32_e32 v171, 0xffff0000, v152
	v_lshlrev_b32_e32 v152, 16, v153
	v_and_b32_e32 v153, 0xffff0000, v153
	v_mul_f32_e32 v6, v95, v95
	v_mul_f32_e32 v7, v85, v85
	v_pk_fma_f32 v[82:83], v[10:11], v[16:17], v[152:153]
	v_pk_fma_f32 v[96:97], v[12:13], v[166:167], v[170:171]
	v_fmac_f32_e32 v6, v94, v94
	v_fmac_f32_e32 v7, v84, v84
	v_add_f32_e32 v6, v6, v7
	v_mul_f32_e32 v7, v97, v97
	v_mul_f32_e32 v8, v83, v83
	v_fmac_f32_e32 v7, v96, v96
	v_fmac_f32_e32 v8, v82, v82
	v_add_f32_e32 v7, v7, v8
	v_add_f32_e32 v6, v6, v7
	v_add_f32_e32 v6, v19, v6
	v_mov_b32_e32 v7, v6
	s_nop 1
	v_permlane16_swap_b32 v7, v6
	s_nop 0
	v_add_u32_e32 v19, 0x80, v189
	s_waitcnt lgkmcnt(0)
	v_add_f32_e32 v6, v6, v7
	v_mov_b32_e32 v7, v6
	s_nop 1
	v_permlane32_swap_b32 v7, v6
	s_nop 0
	s_and_saveexec_b64 s[20:21], vcc
	s_cbranch_execz .LBB0_1543
	v_lshl_add_u32 v8, v19, 4, s5
	s_waitcnt lgkmcnt(0)
	v_add_f32_e32 v6, v6, v7
	ds_write_b32 v8, v6
.LBB0_1543:
	s_or_b64 exec, exec, s[20:21]
	v_add_u32_e32 v150, 0x90, v18
	v_ashrrev_i32_e32 v151, 31, v150
	s_waitcnt lgkmcnt(0)
	s_waitcnt vmcnt(8)
	v_mov_b64_e32 v[6:7], v[216:217]
	v_mov_b64_e32 v[8:9], v[218:219]
	v_mov_b64_e32 v[10:11], v[220:221]
	v_mov_b64_e32 v[12:13], v[222:223]
	v_mov_b64_e32 v[14:15], v[224:225]
	v_mov_b64_e32 v[16:17], v[226:227]
	v_mov_b64_e32 v[152:153], v[228:229]
	v_mov_b64_e32 v[154:155], v[230:231]
	v_pk_mul_f32 v[80:81], v[80:81], s[6:7] op_sel_hi:[1,0]
	v_pk_mul_f32 v[78:79], v[78:79], s[6:7] op_sel_hi:[1,0]
	v_pk_mul_f32 v[76:77], v[76:77], s[6:7] op_sel_hi:[1,0]
	v_pk_mul_f32 v[74:75], v[74:75], s[6:7] op_sel_hi:[1,0]
	v_pk_mul_f32 v[72:73], v[72:73], s[6:7] op_sel_hi:[1,0]
	v_pk_mul_f32 v[78:79], v[78:79], s[2:3] op_sel_hi:[1,0]
	v_pk_mul_f32 v[80:81], v[80:81], s[2:3] op_sel_hi:[1,0]
	v_pk_mul_f32 v[74:75], v[74:75], s[2:3] op_sel_hi:[1,0]
	v_pk_mul_f32 v[76:77], v[76:77], s[2:3] op_sel_hi:[1,0]
	v_pk_mul_f32 v[156:157], v[72:73], s[2:3] op_sel_hi:[1,0]
	v_exp_f32_e32 v72, v78
	v_exp_f32_e32 v73, v79
	v_exp_f32_e32 v78, v80
	v_exp_f32_e32 v79, v81
	v_exp_f32_e32 v74, v74
	v_exp_f32_e32 v75, v75
	v_exp_f32_e32 v76, v76
	v_exp_f32_e32 v77, v77
	v_pk_mul_f32 v[70:71], v[70:71], s[6:7] op_sel_hi:[1,0]
	v_pk_add_f32 v[74:75], v[74:75], 1.0 op_sel_hi:[1,0]
	v_pk_mul_f32 v[70:71], v[70:71], s[2:3] op_sel_hi:[1,0]
	v_pk_add_f32 v[76:77], v[76:77], 1.0 op_sel_hi:[1,0]
	v_exp_f32_e32 v80, v70
	v_exp_f32_e32 v81, v71
	v_pk_add_f32 v[70:71], v[72:73], 1.0 op_sel_hi:[1,0]
	v_pk_add_f32 v[72:73], v[78:79], 1.0 op_sel_hi:[1,0]
	v_rcp_f32_e32 v70, v70
	v_rcp_f32_e32 v71, v71
	v_rcp_f32_e32 v72, v72
	v_rcp_f32_e32 v73, v73
	v_rcp_f32_e32 v78, v74
	v_rcp_f32_e32 v79, v75
	v_rcp_f32_e32 v158, v76
	v_rcp_f32_e32 v159, v77
	v_lshlrev_b32_e32 v162, 16, v10
	v_lshlrev_b32_e32 v76, 16, v6
	v_and_b32_e32 v77, 0xffff0000, v6
	v_lshlrev_b32_e32 v6, 16, v7
	v_and_b32_e32 v7, 0xffff0000, v7
	v_lshlrev_b32_e32 v160, 16, v8
	v_and_b32_e32 v161, 0xffff0000, v8
	v_lshlrev_b32_e32 v8, 16, v9
	v_and_b32_e32 v9, 0xffff0000, v9
	v_and_b32_e32 v163, 0xffff0000, v10
	v_lshlrev_b32_e32 v10, 16, v11
	v_and_b32_e32 v11, 0xffff0000, v11
	v_lshlrev_b32_e32 v164, 16, v12
	v_and_b32_e32 v165, 0xffff0000, v12
	v_lshlrev_b32_e32 v12, 16, v13
	v_and_b32_e32 v13, 0xffff0000, v13
	v_pk_fma_f32 v[74:75], v[72:73], v[6:7], v[10:11]
	v_pk_fma_f32 v[76:77], v[70:71], v[76:77], v[162:163]
	v_pk_fma_f32 v[70:71], v[158:159], v[8:9], v[12:13]
	v_pk_fma_f32 v[72:73], v[78:79], v[160:161], v[164:165]
	v_mul_f32_e32 v6, v77, v77
	v_mul_f32_e32 v7, v75, v75
	v_mul_f32_e32 v8, v73, v73
	v_mul_f32_e32 v9, v71, v71
	v_fmac_f32_e32 v6, v76, v76
	v_fmac_f32_e32 v7, v74, v74
	v_fmac_f32_e32 v8, v72, v72
	v_fmac_f32_e32 v9, v70, v70
	v_add_f32_e32 v6, v6, v7
	v_add_f32_e32 v7, v8, v9
	v_add_f32_e32 v158, v6, v7
	v_exp_f32_e32 v6, v156
	v_exp_f32_e32 v7, v157
	v_pk_mul_f32 v[10:11], v[68:69], s[6:7] op_sel_hi:[1,0]
	v_pk_mul_f32 v[12:13], v[66:67], s[6:7] op_sel_hi:[1,0]
	v_pk_mul_f32 v[10:11], v[10:11], s[2:3] op_sel_hi:[1,0]
	v_pk_mul_f32 v[12:13], v[12:13], s[2:3] op_sel_hi:[1,0]
	v_exp_f32_e32 v10, v10
	v_exp_f32_e32 v12, v12
	v_exp_f32_e32 v13, v13
	v_exp_f32_e32 v11, v11
	v_pk_add_f32 v[8:9], v[80:81], 1.0 op_sel_hi:[1,0]
	v_pk_add_f32 v[6:7], v[6:7], 1.0 op_sel_hi:[1,0]
	v_rcp_f32_e32 v8, v8
	v_rcp_f32_e32 v9, v9
	v_rcp_f32_e32 v6, v6
	v_rcp_f32_e32 v7, v7
	v_pk_add_f32 v[12:13], v[12:13], 1.0 op_sel_hi:[1,0]
	v_pk_add_f32 v[10:11], v[10:11], 1.0 op_sel_hi:[1,0]
	v_rcp_f32_e32 v12, v12
	v_rcp_f32_e32 v10, v10
	v_rcp_f32_e32 v11, v11
	v_rcp_f32_e32 v13, v13
	v_lshlrev_b32_e32 v166, 16, v14
	v_and_b32_e32 v167, 0xffff0000, v14
	v_lshlrev_b32_e32 v14, 16, v15
	v_and_b32_e32 v15, 0xffff0000, v15
	v_lshlrev_b32_e32 v170, 16, v152
	v_and_b32_e32 v171, 0xffff0000, v152
	v_lshlrev_b32_e32 v152, 16, v153
	v_and_b32_e32 v153, 0xffff0000, v153
	v_pk_fma_f32 v[68:69], v[6:7], v[14:15], v[152:153]
	v_pk_fma_f32 v[78:79], v[8:9], v[166:167], v[170:171]
	v_lshlrev_b32_e32 v168, 16, v16
	v_and_b32_e32 v169, 0xffff0000, v16
	v_lshlrev_b32_e32 v16, 16, v17
	v_and_b32_e32 v17, 0xffff0000, v17
	v_lshlrev_b32_e32 v172, 16, v154
	v_and_b32_e32 v173, 0xffff0000, v154
	v_lshlrev_b32_e32 v154, 16, v155
	v_and_b32_e32 v155, 0xffff0000, v155
	v_mul_f32_e32 v6, v79, v79
	v_mul_f32_e32 v7, v69, v69
	v_pk_fma_f32 v[66:67], v[10:11], v[16:17], v[154:155]
	v_pk_fma_f32 v[80:81], v[12:13], v[168:169], v[172:173]
	v_fmac_f32_e32 v6, v78, v78
	v_fmac_f32_e32 v7, v68, v68
	v_add_f32_e32 v6, v6, v7
	v_mul_f32_e32 v7, v81, v81
	v_mul_f32_e32 v8, v67, v67
	v_fmac_f32_e32 v7, v80, v80
	v_fmac_f32_e32 v8, v66, v66
	v_add_f32_e32 v7, v7, v8
	v_add_f32_e32 v6, v6, v7
	v_add_f32_e32 v6, v158, v6
	v_mov_b32_e32 v7, v6
	s_nop 1
	v_permlane16_swap_b32 v7, v6
	s_nop 0
	s_waitcnt lgkmcnt(0)
	v_add_f32_e32 v6, v6, v7
	v_mov_b32_e32 v7, v6
	s_nop 1
	v_permlane32_swap_b32 v7, v6
	s_nop 0
	s_and_saveexec_b64 s[2:3], vcc
	s_cbranch_execz .LBB0_1545
	s_waitcnt lgkmcnt(0)
	v_add_f32_e32 v6, v6, v7
	ds_write_b32 v4, v6 offset:2304
.LBB0_1545:
	s_or_b64 exec, exec, s[2:3]
	v_add_u32_e32 v152, 0xa0, v18
	v_ashrrev_i32_e32 v153, 31, v152
	s_waitcnt lgkmcnt(0)
	s_waitcnt vmcnt(4)
	v_mov_b64_e32 v[6:7], v[232:233]
	v_mov_b64_e32 v[8:9], v[234:235]
	v_mov_b64_e32 v[10:11], v[236:237]
	v_mov_b64_e32 v[12:13], v[238:239]
	v_mov_b64_e32 v[14:15], v[240:241]
	v_mov_b64_e32 v[16:17], v[242:243]
	v_mov_b64_e32 v[154:155], v[244:245]
	v_mov_b64_e32 v[156:157], v[246:247]
	s_mov_b32 s2, 0xbfb8aa3b
	v_pk_mul_f32 v[64:65], v[64:65], s[6:7] op_sel_hi:[1,0]
	v_pk_mul_f32 v[62:63], v[62:63], s[6:7] op_sel_hi:[1,0]
	v_pk_mul_f32 v[60:61], v[60:61], s[6:7] op_sel_hi:[1,0]
	v_pk_mul_f32 v[58:59], v[58:59], s[6:7] op_sel_hi:[1,0]
	v_pk_mul_f32 v[158:159], v[56:57], s[6:7] op_sel_hi:[1,0]
	v_pk_mul_f32 v[54:55], v[54:55], s[6:7] op_sel_hi:[1,0]
	v_pk_mul_f32 v[56:57], v[62:63], s[2:3] op_sel_hi:[1,0]
	v_pk_mul_f32 v[62:63], v[64:65], s[2:3] op_sel_hi:[1,0]
	v_pk_mul_f32 v[58:59], v[58:59], s[2:3] op_sel_hi:[1,0]
	v_pk_mul_f32 v[60:61], v[60:61], s[2:3] op_sel_hi:[1,0]
	v_pk_mul_f32 v[64:65], v[54:55], s[2:3] op_sel_hi:[1,0]
	v_exp_f32_e32 v54, v56
	v_exp_f32_e32 v55, v57
	v_exp_f32_e32 v56, v62
	v_exp_f32_e32 v57, v63
	v_exp_f32_e32 v58, v58
	v_exp_f32_e32 v59, v59
	v_exp_f32_e32 v60, v60
	v_exp_f32_e32 v61, v61
	v_pk_add_f32 v[54:55], v[54:55], 1.0 op_sel_hi:[1,0]
	v_pk_add_f32 v[56:57], v[56:57], 1.0 op_sel_hi:[1,0]
	v_pk_add_f32 v[58:59], v[58:59], 1.0 op_sel_hi:[1,0]
	v_pk_add_f32 v[60:61], v[60:61], 1.0 op_sel_hi:[1,0]
	v_rcp_f32_e32 v54, v54
	v_rcp_f32_e32 v55, v55
	v_rcp_f32_e32 v56, v56
	v_rcp_f32_e32 v57, v57
	v_rcp_f32_e32 v160, v58
	v_rcp_f32_e32 v161, v59
	v_rcp_f32_e32 v162, v60
	v_rcp_f32_e32 v163, v61
	v_exp_f32_e32 v62, v64
	v_exp_f32_e32 v63, v65
	v_lshlrev_b32_e32 v166, 16, v10
	v_lshlrev_b32_e32 v60, 16, v6
	v_and_b32_e32 v61, 0xffff0000, v6
	v_lshlrev_b32_e32 v6, 16, v7
	v_and_b32_e32 v7, 0xffff0000, v7
	v_lshlrev_b32_e32 v164, 16, v8
	v_and_b32_e32 v165, 0xffff0000, v8
	v_lshlrev_b32_e32 v8, 16, v9
	v_and_b32_e32 v9, 0xffff0000, v9
	v_and_b32_e32 v167, 0xffff0000, v10
	v_lshlrev_b32_e32 v10, 16, v11
	v_and_b32_e32 v11, 0xffff0000, v11
	v_lshlrev_b32_e32 v168, 16, v12
	v_and_b32_e32 v169, 0xffff0000, v12
	v_lshlrev_b32_e32 v12, 16, v13
	v_and_b32_e32 v13, 0xffff0000, v13
	v_pk_fma_f32 v[58:59], v[56:57], v[6:7], v[10:11]
	v_pk_fma_f32 v[60:61], v[54:55], v[60:61], v[166:167]
	v_pk_fma_f32 v[54:55], v[162:163], v[8:9], v[12:13]
	v_pk_fma_f32 v[56:57], v[160:161], v[164:165], v[168:169]
	v_mul_f32_e32 v6, v61, v61
	v_mul_f32_e32 v7, v59, v59
	v_mul_f32_e32 v8, v57, v57
	v_mul_f32_e32 v9, v55, v55
	v_fmac_f32_e32 v6, v60, v60
	v_fmac_f32_e32 v7, v58, v58
	v_fmac_f32_e32 v8, v56, v56
	v_fmac_f32_e32 v9, v54, v54
	v_add_f32_e32 v6, v6, v7
	v_add_f32_e32 v7, v8, v9
	v_add_f32_e32 v160, v6, v7
	v_pk_mul_f32 v[6:7], v[158:159], s[2:3] op_sel_hi:[1,0]
	v_pk_mul_f32 v[10:11], v[52:53], s[6:7] op_sel_hi:[1,0]
	v_exp_f32_e32 v6, v6
	v_exp_f32_e32 v7, v7
	v_pk_mul_f32 v[12:13], v[50:51], s[6:7] op_sel_hi:[1,0]
	v_pk_mul_f32 v[10:11], v[10:11], s[2:3] op_sel_hi:[1,0]
	v_pk_mul_f32 v[12:13], v[12:13], s[2:3] op_sel_hi:[1,0]
	v_exp_f32_e32 v10, v10
	v_exp_f32_e32 v12, v12
	v_exp_f32_e32 v13, v13
	v_exp_f32_e32 v11, v11
	v_pk_add_f32 v[8:9], v[62:63], 1.0 op_sel_hi:[1,0]
	v_pk_add_f32 v[6:7], v[6:7], 1.0 op_sel_hi:[1,0]
	v_rcp_f32_e32 v8, v8
	v_rcp_f32_e32 v9, v9
	v_rcp_f32_e32 v6, v6
	v_rcp_f32_e32 v7, v7
	v_pk_add_f32 v[12:13], v[12:13], 1.0 op_sel_hi:[1,0]
	v_pk_add_f32 v[10:11], v[10:11], 1.0 op_sel_hi:[1,0]
	v_rcp_f32_e32 v12, v12
	v_rcp_f32_e32 v10, v10
	v_rcp_f32_e32 v11, v11
	v_rcp_f32_e32 v13, v13
	v_lshlrev_b32_e32 v170, 16, v14
	v_and_b32_e32 v171, 0xffff0000, v14
	v_lshlrev_b32_e32 v14, 16, v15
	v_and_b32_e32 v15, 0xffff0000, v15
	v_lshlrev_b32_e32 v174, 16, v154
	v_and_b32_e32 v175, 0xffff0000, v154
	v_lshlrev_b32_e32 v154, 16, v155
	v_and_b32_e32 v155, 0xffff0000, v155
	v_pk_fma_f32 v[52:53], v[6:7], v[14:15], v[154:155]
	v_pk_fma_f32 v[62:63], v[8:9], v[170:171], v[174:175]
	v_lshlrev_b32_e32 v172, 16, v16
	v_and_b32_e32 v173, 0xffff0000, v16
	v_lshlrev_b32_e32 v16, 16, v17
	v_and_b32_e32 v17, 0xffff0000, v17
	v_lshlrev_b32_e32 v176, 16, v156
	v_and_b32_e32 v177, 0xffff0000, v156
	v_lshlrev_b32_e32 v156, 16, v157
	v_and_b32_e32 v157, 0xffff0000, v157
	v_mul_f32_e32 v6, v63, v63
	v_mul_f32_e32 v7, v53, v53
	v_pk_fma_f32 v[50:51], v[10:11], v[16:17], v[156:157]
	v_pk_fma_f32 v[64:65], v[12:13], v[172:173], v[176:177]
	v_fmac_f32_e32 v6, v62, v62
	v_fmac_f32_e32 v7, v52, v52
	v_add_f32_e32 v6, v6, v7
	v_mul_f32_e32 v7, v65, v65
	v_mul_f32_e32 v8, v51, v51
	v_fmac_f32_e32 v7, v64, v64
	v_fmac_f32_e32 v8, v50, v50
	v_add_f32_e32 v7, v7, v8
	v_add_f32_e32 v6, v6, v7
	v_add_f32_e32 v6, v160, v6
	v_mov_b32_e32 v7, v6
	s_nop 1
	v_permlane16_swap_b32 v7, v6
	s_nop 0
	s_waitcnt lgkmcnt(0)
	v_add_f32_e32 v6, v6, v7
	v_mov_b32_e32 v7, v6
	s_nop 1
	v_permlane32_swap_b32 v7, v6
	s_nop 0
	s_and_saveexec_b64 s[20:21], vcc
	s_cbranch_execz .LBB0_1547
	s_waitcnt lgkmcnt(0)
	v_add_f32_e32 v6, v6, v7
	ds_write_b32 v4, v6 offset:2560
.LBB0_1547:
	s_or_b64 exec, exec, s[20:21]
	v_add_u32_e32 v154, 0xb0, v18
	v_ashrrev_i32_e32 v155, 31, v154
	s_waitcnt lgkmcnt(0)
	s_waitcnt vmcnt(0)
	v_mov_b64_e32 v[6:7], v[200:201]
	v_mov_b64_e32 v[8:9], v[202:203]
	v_mov_b64_e32 v[10:11], v[204:205]
	v_mov_b64_e32 v[12:13], v[206:207]
	v_mov_b64_e32 v[14:15], v[208:209]
	v_mov_b64_e32 v[16:17], v[210:211]
	v_mov_b64_e32 v[156:157], v[212:213]
	v_mov_b64_e32 v[158:159], v[214:215]
	v_pk_mul_f32 v[48:49], v[48:49], s[6:7] op_sel_hi:[1,0]
	v_pk_mul_f32 v[46:47], v[46:47], s[6:7] op_sel_hi:[1,0]
	v_pk_mul_f32 v[44:45], v[44:45], s[6:7] op_sel_hi:[1,0]
	v_pk_mul_f32 v[42:43], v[42:43], s[6:7] op_sel_hi:[1,0]
	v_pk_mul_f32 v[40:41], v[40:41], s[6:7] op_sel_hi:[1,0]
	v_pk_mul_f32 v[46:47], v[46:47], s[2:3] op_sel_hi:[1,0]
	v_pk_mul_f32 v[48:49], v[48:49], s[2:3] op_sel_hi:[1,0]
	v_pk_mul_f32 v[42:43], v[42:43], s[2:3] op_sel_hi:[1,0]
	v_pk_mul_f32 v[44:45], v[44:45], s[2:3] op_sel_hi:[1,0]
	v_pk_mul_f32 v[160:161], v[40:41], s[2:3] op_sel_hi:[1,0]
	v_exp_f32_e32 v40, v46
	v_exp_f32_e32 v41, v47
	v_exp_f32_e32 v46, v48
	v_exp_f32_e32 v47, v49
	v_exp_f32_e32 v42, v42
	v_exp_f32_e32 v43, v43
	v_exp_f32_e32 v44, v44
	v_exp_f32_e32 v45, v45
	v_pk_mul_f32 v[38:39], v[38:39], s[6:7] op_sel_hi:[1,0]
	v_pk_add_f32 v[42:43], v[42:43], 1.0 op_sel_hi:[1,0]
	v_pk_mul_f32 v[38:39], v[38:39], s[2:3] op_sel_hi:[1,0]
	v_pk_add_f32 v[44:45], v[44:45], 1.0 op_sel_hi:[1,0]
	v_exp_f32_e32 v48, v38
	v_exp_f32_e32 v49, v39
	v_pk_add_f32 v[38:39], v[40:41], 1.0 op_sel_hi:[1,0]
	v_pk_add_f32 v[40:41], v[46:47], 1.0 op_sel_hi:[1,0]
	v_rcp_f32_e32 v38, v38
	v_rcp_f32_e32 v39, v39
	v_rcp_f32_e32 v40, v40
	v_rcp_f32_e32 v41, v41
	v_rcp_f32_e32 v46, v42
	v_rcp_f32_e32 v47, v43
	v_rcp_f32_e32 v162, v44
	v_rcp_f32_e32 v163, v45
	v_lshlrev_b32_e32 v166, 16, v10
	v_lshlrev_b32_e32 v44, 16, v6
	v_and_b32_e32 v45, 0xffff0000, v6
	v_lshlrev_b32_e32 v6, 16, v7
	v_and_b32_e32 v7, 0xffff0000, v7
	v_lshlrev_b32_e32 v164, 16, v8
	v_and_b32_e32 v165, 0xffff0000, v8
	v_lshlrev_b32_e32 v8, 16, v9
	v_and_b32_e32 v9, 0xffff0000, v9
	v_and_b32_e32 v167, 0xffff0000, v10
	v_lshlrev_b32_e32 v10, 16, v11
	v_and_b32_e32 v11, 0xffff0000, v11
	v_lshlrev_b32_e32 v168, 16, v12
	v_and_b32_e32 v169, 0xffff0000, v12
	v_lshlrev_b32_e32 v12, 16, v13
	v_and_b32_e32 v13, 0xffff0000, v13
	v_pk_fma_f32 v[42:43], v[40:41], v[6:7], v[10:11]
	v_pk_fma_f32 v[44:45], v[38:39], v[44:45], v[166:167]
	v_pk_fma_f32 v[38:39], v[162:163], v[8:9], v[12:13]
	v_pk_fma_f32 v[40:41], v[46:47], v[164:165], v[168:169]
	v_mul_f32_e32 v6, v45, v45
	v_mul_f32_e32 v7, v43, v43
	v_mul_f32_e32 v8, v41, v41
	v_mul_f32_e32 v9, v39, v39
	v_fmac_f32_e32 v6, v44, v44
	v_fmac_f32_e32 v7, v42, v42
	v_fmac_f32_e32 v8, v40, v40
	v_fmac_f32_e32 v9, v38, v38
	v_add_f32_e32 v6, v6, v7
	v_add_f32_e32 v7, v8, v9
	v_add_f32_e32 v162, v6, v7
	v_exp_f32_e32 v6, v160
	v_exp_f32_e32 v7, v161
	v_pk_mul_f32 v[10:11], v[36:37], s[6:7] op_sel_hi:[1,0]
	v_pk_mul_f32 v[12:13], v[34:35], s[6:7] op_sel_hi:[1,0]
	v_pk_mul_f32 v[10:11], v[10:11], s[2:3] op_sel_hi:[1,0]
	v_pk_mul_f32 v[12:13], v[12:13], s[2:3] op_sel_hi:[1,0]
	v_exp_f32_e32 v10, v10
	v_exp_f32_e32 v12, v12
	v_exp_f32_e32 v13, v13
	v_exp_f32_e32 v11, v11
	v_pk_add_f32 v[8:9], v[48:49], 1.0 op_sel_hi:[1,0]
	v_pk_add_f32 v[6:7], v[6:7], 1.0 op_sel_hi:[1,0]
	v_rcp_f32_e32 v8, v8
	v_rcp_f32_e32 v9, v9
	v_rcp_f32_e32 v6, v6
	v_rcp_f32_e32 v7, v7
	v_pk_add_f32 v[12:13], v[12:13], 1.0 op_sel_hi:[1,0]
	v_pk_add_f32 v[10:11], v[10:11], 1.0 op_sel_hi:[1,0]
	v_rcp_f32_e32 v12, v12
	v_rcp_f32_e32 v10, v10
	v_rcp_f32_e32 v11, v11
	v_rcp_f32_e32 v13, v13
	v_lshlrev_b32_e32 v170, 16, v14
	v_and_b32_e32 v171, 0xffff0000, v14
	v_lshlrev_b32_e32 v14, 16, v15
	v_and_b32_e32 v15, 0xffff0000, v15
	v_lshlrev_b32_e32 v174, 16, v156
	v_and_b32_e32 v175, 0xffff0000, v156
	v_lshlrev_b32_e32 v156, 16, v157
	v_and_b32_e32 v157, 0xffff0000, v157
	v_pk_fma_f32 v[36:37], v[6:7], v[14:15], v[156:157]
	v_pk_fma_f32 v[46:47], v[8:9], v[170:171], v[174:175]
	v_lshlrev_b32_e32 v172, 16, v16
	v_and_b32_e32 v173, 0xffff0000, v16
	v_lshlrev_b32_e32 v16, 16, v17
	v_and_b32_e32 v17, 0xffff0000, v17
	v_lshlrev_b32_e32 v176, 16, v158
	v_and_b32_e32 v177, 0xffff0000, v158
	v_lshlrev_b32_e32 v158, 16, v159
	v_and_b32_e32 v159, 0xffff0000, v159
	v_mul_f32_e32 v6, v47, v47
	v_mul_f32_e32 v7, v37, v37
	v_pk_fma_f32 v[34:35], v[10:11], v[16:17], v[158:159]
	v_pk_fma_f32 v[48:49], v[12:13], v[172:173], v[176:177]
	v_fmac_f32_e32 v6, v46, v46
	v_fmac_f32_e32 v7, v36, v36
	v_add_f32_e32 v6, v6, v7
	v_mul_f32_e32 v7, v49, v49
	v_mul_f32_e32 v8, v35, v35
	v_fmac_f32_e32 v7, v48, v48
	v_fmac_f32_e32 v8, v34, v34
	v_add_f32_e32 v7, v7, v8
	v_add_f32_e32 v6, v6, v7
	v_add_f32_e32 v6, v162, v6
	v_mov_b32_e32 v1, v6
	s_nop 1
	v_permlane16_swap_b32 v1, v6
	s_nop 0
	s_waitcnt lgkmcnt(0)
	v_add_f32_e32 v1, v6, v1
	v_mov_b32_e32 v5, v1
	s_nop 1
	v_permlane32_swap_b32 v5, v1
	s_nop 0
	s_and_saveexec_b64 s[2:3], vcc
	s_cbranch_execz .LBB0_1549
	s_waitcnt lgkmcnt(0)
	v_add_f32_e32 v1, v1, v5
	ds_write_b32 v4, v1 offset:2816
